# sc1 write-through on q/k/v and y 16-byte stores (no bulk L2 flush at kernel end)
# speedup vs baseline: 1.0100x; 1.0100x over previous
.LBB2_15:
	v_mov_b32_e32 v133, 0
	s_waitcnt lgkmcnt(0)
	global_load_dwordx2 v[130:131], v133, s[6:7]
	s_lshl_b32 s10, s24, 7
	v_lshlrev_b32_e32 v3, 5, v0
	v_or_b32_e32 v2, s10, v1
	s_lshl_b32 s6, s3, 8
	v_and_b32_e32 v132, 0x1e0, v3
	v_ashrrev_i32_e32 v3, 31, v2
	s_ashr_i32 s7, s6, 31
	v_lshlrev_b64 v[2:3], 13, v[2:3]
	s_or_b32 s16, s6, 0x80
	s_lshl_b64 s[6:7], s[6:7], 2
	v_lshl_add_u64 v[2:3], s[14:15], 0, v[2:3]
	v_lshl_add_u64 v[2:3], v[2:3], 0, s[6:7]
	v_lshl_add_u64 v[2:3], v[2:3], 0, v[132:133]
	v_lshl_or_b32 v6, v122, 2, s25
	global_load_dwordx4 v[122:125], v[2:3], off offset:16 nt
	global_load_dwordx4 v[126:129], v[2:3], off nt
	v_or_b32_e32 v4, 0x200, v0
	v_or_b32_e32 v135, 64, v1
	v_or_b32_e32 v5, 0x600, v0
	s_movk_i32 s11, 0x110
	v_lshrrev_b32_e32 v137, 4, v4
	v_or_b32_e32 v4, s10, v135
	v_lshrrev_b32_e32 v136, 4, v5
	s_lshl_b32 s18, s26, 1
	v_lshl_add_u32 v138, v134, 2, 0
	v_mul_lo_u32 v7, v6, s11
	v_or_b32_e32 v6, s10, v137
	v_ashrrev_i32_e32 v5, 31, v4
	v_or_b32_e32 v8, s10, v136
	v_add3_u32 v139, v138, s18, v7
	v_ashrrev_i32_e32 v7, 31, v6
	v_lshlrev_b64 v[4:5], 13, v[4:5]
	v_ashrrev_i32_e32 v9, 31, v8
	v_lshlrev_b64 v[6:7], 13, v[6:7]
	v_lshl_add_u64 v[4:5], s[14:15], 0, v[4:5]
	v_lshlrev_b64 v[8:9], 13, v[8:9]
	s_ashr_i32 s17, s16, 31
	v_lshl_add_u64 v[6:7], s[14:15], 0, v[6:7]
	v_lshl_add_u64 v[4:5], v[4:5], 0, s[6:7]
	v_lshl_add_u64 v[8:9], s[14:15], 0, v[8:9]
	v_lshl_add_u64 v[6:7], v[6:7], 0, s[6:7]
	v_lshl_add_u64 v[4:5], v[4:5], 0, v[132:133]
	v_lshl_add_u64 v[10:11], v[8:9], 0, s[6:7]
	v_lshl_add_u64 v[8:9], s[16:17], 2, v[8:9]
	v_lshl_add_u64 v[6:7], v[6:7], 0, v[132:133]
	global_load_dwordx4 v[42:45], v[4:5], off offset:16 nt
	global_load_dwordx4 v[46:49], v[4:5], off nt
	v_lshl_add_u64 v[18:19], v[10:11], 0, v[132:133]
	v_lshl_add_u64 v[8:9], v[8:9], 0, v[132:133]
	global_load_dwordx4 v[26:29], v[2:3], off offset:528 nt
	global_load_dwordx4 v[30:33], v[2:3], off offset:512 nt
	global_load_dwordx4 v[10:13], v[4:5], off offset:528 nt
	global_load_dwordx4 v[14:17], v[4:5], off offset:512 nt
	global_load_dwordx4 v[50:53], v[6:7], off offset:16 nt
	global_load_dwordx4 v[54:57], v[6:7], off nt
	global_load_dwordx4 v[34:37], v[18:19], off offset:16 nt
	global_load_dwordx4 v[38:41], v[18:19], off nt
	s_nop 0
	global_load_dwordx4 v[18:21], v[6:7], off offset:528 nt
	global_load_dwordx4 v[22:25], v[6:7], off offset:512 nt
	global_load_dwordx4 v[2:5], v[8:9], off offset:16 nt
	s_nop 0
	global_load_dwordx4 v[6:9], v[8:9], off nt
	s_waitcnt vmcnt(17)
	s_barrier
	s_lshl_b32 s6, s3, 1
	v_lshlrev_b32_e32 v132, 4, v134
	s_ashr_i32 s7, s6, 31
	s_ashr_i32 s3, s10, 31
	s_waitcnt vmcnt(16)
	v_mul_f32_e32 v86, v86, v130
	v_mul_f32_e32 v82, v82, v130
	v_mul_f32_e32 v118, v118, v130
	v_mul_f32_e32 v114, v114, v130
	v_mul_f32_e32 v119, v119, v130
	v_mul_f32_e32 v115, v115, v130
	v_cvt_pk_f16_f32 v82, v86, v82
	v_mul_f32_e32 v86, v87, v130
	v_mul_f32_e32 v83, v83, v130
	v_mul_f32_e32 v120, v120, v130
	v_mul_f32_e32 v116, v116, v130
	v_mul_f32_e32 v121, v121, v130
	v_mul_f32_e32 v117, v117, v130
	v_cvt_pk_f16_f32 v114, v118, v114
	v_cvt_pk_f16_f32 v115, v119, v115
	v_mul_f32_e32 v102, v102, v130
	v_mul_f32_e32 v98, v98, v130
	v_mul_f32_e32 v94, v94, v130
	v_mul_f32_e32 v90, v90, v130
	v_cvt_pk_f16_f32 v83, v86, v83
	v_add_u32_e32 v86, 0x8800, v139
	v_mul_f32_e32 v78, v78, v130
	v_mul_f32_e32 v74, v74, v130
	v_mul_f32_e32 v70, v70, v130
	v_mul_f32_e32 v66, v66, v130
	v_mul_f32_e32 v62, v62, v130
	v_mul_f32_e32 v58, v130, v58
	v_mul_f32_e32 v110, v110, v130
	v_mul_f32_e32 v106, v106, v130
	v_mul_f32_e32 v111, v111, v130
	v_cvt_pk_f16_f32 v116, v120, v116
	v_cvt_pk_f16_f32 v117, v121, v117
	ds_write2_b32 v139, v114, v115 offset1:68
	ds_write2_b32 v139, v116, v117 offset0:136 offset1:204
	v_mul_f32_e32 v107, v107, v130
	v_cvt_pk_f16_f32 v98, v102, v98
	v_mul_f32_e32 v102, v103, v130
	v_mul_f32_e32 v99, v99, v130
	v_cvt_pk_f16_f32 v90, v94, v90
	v_mul_f32_e32 v94, v95, v130
	v_mul_f32_e32 v91, v91, v130
	ds_write2_b32 v86, v82, v83 offset1:68
	v_mul_f32_e32 v82, v88, v130
	v_mul_f32_e32 v83, v84, v130
	v_cvt_pk_f16_f32 v74, v78, v74
	v_mul_f32_e32 v78, v79, v130
	v_mul_f32_e32 v75, v75, v130
	v_cvt_pk_f16_f32 v66, v70, v66
	v_mul_f32_e32 v70, v71, v130
	v_mul_f32_e32 v67, v67, v130
	v_cvt_pk_f16_f32 v58, v62, v58
	v_mul_f32_e32 v62, v63, v130
	v_mul_f32_e32 v59, v130, v59
	v_cvt_pk_f16_f32 v106, v110, v106
	v_cvt_pk_f16_f32 v107, v111, v107
	v_add_u32_e32 v110, 0x1000, v139
	v_cvt_pk_f16_f32 v99, v102, v99
	v_add_u32_e32 v102, 0x2000, v139
	v_cvt_pk_f16_f32 v91, v94, v91
	v_add_u32_e32 v94, 0x3200, v139
	v_cvt_pk_f16_f32 v82, v82, v83
	v_mul_f32_e32 v83, v89, v130
	v_mul_f32_e32 v84, v85, v130
	v_cvt_pk_f16_f32 v75, v78, v75
	v_add_u32_e32 v78, 0x9800, v139
	v_cvt_pk_f16_f32 v67, v70, v67
	v_add_u32_e32 v70, 0xa800, v139
	v_cvt_pk_f16_f32 v59, v62, v59
	v_add_u32_e32 v62, 0xba00, v139
	ds_write2_b32 v110, v106, v107 offset0:64 offset1:132
	v_mul_f32_e32 v106, v112, v130
	v_mul_f32_e32 v107, v108, v130
	ds_write2_b32 v102, v98, v99 offset0:128 offset1:196
	v_mul_f32_e32 v98, v104, v130
	v_mul_f32_e32 v99, v100, v130
	ds_write2_b32 v94, v90, v91 offset0:64 offset1:132
	v_mul_f32_e32 v90, v96, v130
	v_mul_f32_e32 v91, v92, v130
	v_cvt_pk_f16_f32 v83, v83, v84
	ds_write2_b32 v78, v74, v75 offset0:64 offset1:132
	v_mul_f32_e32 v74, v80, v130
	v_mul_f32_e32 v75, v76, v130
	ds_write2_b32 v70, v66, v67 offset0:128 offset1:196
	v_mul_f32_e32 v66, v72, v130
	v_mul_f32_e32 v67, v68, v130
	ds_write2_b32 v62, v58, v59 offset0:64 offset1:132
	v_mul_f32_e32 v58, v64, v130
	v_mul_f32_e32 v59, v130, v60
	v_cvt_pk_f16_f32 v106, v106, v107
	v_mul_f32_e32 v107, v113, v130
	v_mul_f32_e32 v108, v109, v130
	v_cvt_pk_f16_f32 v98, v98, v99
	v_mul_f32_e32 v99, v105, v130
	v_mul_f32_e32 v100, v101, v130
	v_cvt_pk_f16_f32 v90, v90, v91
	v_mul_f32_e32 v91, v97, v130
	v_mul_f32_e32 v92, v93, v130
	ds_write2_b32 v86, v82, v83 offset0:136 offset1:204
	v_cvt_pk_f16_f32 v74, v74, v75
	v_mul_f32_e32 v75, v81, v130
	v_mul_f32_e32 v76, v77, v130
	v_cvt_pk_f16_f32 v66, v66, v67
	v_mul_f32_e32 v67, v73, v130
	v_mul_f32_e32 v68, v69, v130
	v_cvt_pk_f16_f32 v58, v58, v59
	v_mul_f32_e32 v59, v65, v130
	v_mul_f32_e32 v60, v130, v61
	v_mad_u32_u24 v82, v134, 12, v138
	v_cvt_pk_f16_f32 v107, v107, v108
	v_add_u32_e32 v108, 0x1200, v139
	v_cvt_pk_f16_f32 v99, v99, v100
	v_add_u32_e32 v100, 0x2400, v139
	v_cvt_pk_f16_f32 v91, v91, v92
	v_add_u32_e32 v92, 0x3400, v139
	v_cvt_pk_f16_f32 v75, v75, v76
	v_add_u32_e32 v76, 0x9a00, v139
	v_cvt_pk_f16_f32 v67, v67, v68
	v_add_u32_e32 v68, 0xac00, v139
	v_cvt_pk_f16_f32 v59, v59, v60
	v_add_u32_e32 v60, 0xbc00, v139
	v_mad_u32_u24 v83, v1, s11, v82
	ds_write2_b32 v108, v106, v107 offset0:72 offset1:140
	ds_write2_b32 v100, v98, v99 offset0:8 offset1:76
	ds_write2_b32 v92, v90, v91 offset0:72 offset1:140
	ds_write2_b32 v76, v74, v75 offset0:72 offset1:140
	ds_write2_b32 v68, v66, v67 offset0:8 offset1:76
	ds_write2_b32 v60, v58, v59 offset0:72 offset1:140
	s_waitcnt lgkmcnt(0)
	s_barrier
	ds_read_b128 v[58:61], v83
	v_mad_u32_u24 v76, v137, s11, v82
	ds_read_b128 v[62:65], v83 offset:17408
	s_waitcnt lgkmcnt(1)
	v_cvt_f32_f16_e32 v66, v58
	v_cvt_f32_f16_sdwa v67, v58 dst_sel:DWORD dst_unused:UNUSED_PAD src0_sel:WORD_1
	v_cvt_f32_f16_e32 v68, v59
	v_cvt_f32_f16_sdwa v69, v59 dst_sel:DWORD dst_unused:UNUSED_PAD src0_sel:WORD_1
	v_cvt_f32_f16_e32 v70, v60
	v_cvt_f32_f16_sdwa v71, v60 dst_sel:DWORD dst_unused:UNUSED_PAD src0_sel:WORD_1
	v_cvt_f32_f16_e32 v60, v61
	v_cvt_f32_f16_sdwa v61, v61 dst_sel:DWORD dst_unused:UNUSED_PAD src0_sel:WORD_1
	v_lshl_add_u64 v[58:59], s[12:13], 0, v[132:133]
	s_waitcnt vmcnt(14)
	v_pk_fma_f32 v[66:67], v[130:131], v[126:127], v[66:67] op_sel:[1,0,0]
	v_pk_fma_f32 v[68:69], v[130:131], v[128:129], v[68:69] op_sel:[1,0,0]
	s_lshl_b64 s[12:13], s[6:7], 12
	v_cvt_pk_f16_f32 v66, v66, v67
	v_cvt_pk_f16_f32 v67, v68, v69
	v_pk_fma_f32 v[68:69], v[130:131], v[122:123], v[70:71] op_sel:[1,0,0]
	s_add_u32 s7, s12, s10
	ds_read_b128 v[70:73], v76
	v_pk_fma_f32 v[60:61], v[130:131], v[124:125], v[60:61] op_sel:[1,0,0]
	s_addc_u32 s12, s13, s3
	v_cvt_pk_f16_f32 v68, v68, v69
	v_cvt_pk_f16_f32 v69, v60, v61
	v_or_b32_e32 v60, s7, v1
	v_mov_b32_e32 v61, s12
	v_lshlrev_b64 v[74:75], 8, v[60:61]
	v_lshl_add_u64 v[78:79], v[58:59], 0, v[74:75]
	s_waitcnt lgkmcnt(0)
	v_cvt_f32_f16_e32 v80, v70
	v_cvt_f32_f16_sdwa v81, v70 dst_sel:DWORD dst_unused:UNUSED_PAD src0_sel:WORD_1
	v_cvt_f32_f16_e32 v70, v71
	v_cvt_f32_f16_sdwa v71, v71 dst_sel:DWORD dst_unused:UNUSED_PAD src0_sel:WORD_1
	global_store_dwordx4 v[78:79], v[66:69], off sc1
	s_waitcnt vmcnt(7)
	v_pk_fma_f32 v[54:55], v[130:131], v[54:55], v[80:81] op_sel:[1,0,0]
	v_or_b32_e32 v60, s7, v137
	v_cvt_f32_f16_e32 v66, v72
	v_cvt_f32_f16_sdwa v67, v72 dst_sel:DWORD dst_unused:UNUSED_PAD src0_sel:WORD_1
	v_cvt_f32_f16_e32 v68, v73
	v_cvt_f32_f16_sdwa v69, v73 dst_sel:DWORD dst_unused:UNUSED_PAD src0_sel:WORD_1
	v_pk_fma_f32 v[56:57], v[130:131], v[56:57], v[70:71] op_sel:[1,0,0]
	v_pk_fma_f32 v[50:51], v[130:131], v[50:51], v[66:67] op_sel:[1,0,0]
	v_cvt_pk_f16_f32 v54, v54, v55
	v_cvt_pk_f16_f32 v55, v56, v57
	v_cvt_pk_f16_f32 v56, v50, v51
	v_pk_fma_f32 v[50:51], v[130:131], v[52:53], v[68:69] op_sel:[1,0,0]
	v_cvt_f32_f16_e32 v52, v62
	v_cvt_f32_f16_sdwa v53, v62 dst_sel:DWORD dst_unused:UNUSED_PAD src0_sel:WORD_1
	v_cvt_pk_f16_f32 v57, v50, v51
	v_lshlrev_b64 v[50:51], 8, v[60:61]
	v_lshl_add_u64 v[50:51], v[58:59], 0, v[50:51]
	v_cvt_f32_f16_e32 v62, v63
	v_cvt_f32_f16_sdwa v63, v63 dst_sel:DWORD dst_unused:UNUSED_PAD src0_sel:WORD_1
	global_store_dwordx4 v[50:51], v[54:57], off sc1
	v_cvt_f32_f16_e32 v50, v64
	v_cvt_f32_f16_sdwa v51, v64 dst_sel:DWORD dst_unused:UNUSED_PAD src0_sel:WORD_1
	v_pk_fma_f32 v[46:47], v[130:131], v[46:47], v[52:53] op_sel:[1,0,0]
	v_cvt_f32_f16_e32 v52, v65
	v_cvt_f32_f16_sdwa v53, v65 dst_sel:DWORD dst_unused:UNUSED_PAD src0_sel:WORD_1
	v_pk_fma_f32 v[48:49], v[130:131], v[48:49], v[62:63] op_sel:[1,0,0]
	v_pk_fma_f32 v[42:43], v[130:131], v[42:43], v[50:51] op_sel:[1,0,0]
	v_cvt_pk_f16_f32 v46, v46, v47
	v_cvt_pk_f16_f32 v47, v48, v49
	v_cvt_pk_f16_f32 v48, v42, v43
	v_pk_fma_f32 v[42:43], v[130:131], v[44:45], v[52:53] op_sel:[1,0,0]
	v_or_b32_e32 v60, s7, v135
	v_cvt_pk_f16_f32 v49, v42, v43
	v_mad_u32_u24 v42, v136, s11, v82
	ds_read_b128 v[42:45], v42
	v_lshlrev_b64 v[50:51], 8, v[60:61]
	v_lshl_add_u64 v[54:55], v[58:59], 0, v[50:51]
	v_or_b32_e32 v50, 0x80, v136
	v_mad_u32_u24 v50, v50, s11, v82
	ds_read_b128 v[50:53], v50
	s_waitcnt lgkmcnt(1)
	v_cvt_f32_f16_e32 v56, v42
	v_cvt_f32_f16_sdwa v57, v42 dst_sel:DWORD dst_unused:UNUSED_PAD src0_sel:WORD_1
	v_cvt_f32_f16_e32 v42, v43
	v_cvt_f32_f16_sdwa v43, v43 dst_sel:DWORD dst_unused:UNUSED_PAD src0_sel:WORD_1
	ds_read_b128 v[74:77], v76 offset:34816
	s_waitcnt vmcnt(6)
	v_pk_fma_f32 v[38:39], v[130:131], v[38:39], v[56:57] op_sel:[1,0,0]
	v_or_b32_e32 v60, s7, v136
	v_pk_fma_f32 v[40:41], v[130:131], v[40:41], v[42:43] op_sel:[1,0,0]
	v_cvt_f32_f16_e32 v42, v44
	v_cvt_f32_f16_sdwa v43, v44 dst_sel:DWORD dst_unused:UNUSED_PAD src0_sel:WORD_1
	v_cvt_f32_f16_e32 v44, v45
	v_cvt_f32_f16_sdwa v45, v45 dst_sel:DWORD dst_unused:UNUSED_PAD src0_sel:WORD_1
	v_cvt_pk_f16_f32 v38, v38, v39
	v_pk_fma_f32 v[34:35], v[130:131], v[34:35], v[42:43] op_sel:[1,0,0]
	v_cvt_pk_f16_f32 v39, v40, v41
	v_cvt_pk_f16_f32 v40, v34, v35
	v_pk_fma_f32 v[34:35], v[130:131], v[36:37], v[44:45] op_sel:[1,0,0]
	v_lshlrev_b64 v[42:43], 8, v[60:61]
	v_cvt_pk_f16_f32 v41, v34, v35
	ds_read_b128 v[34:37], v83 offset:34816
	v_lshl_add_u64 v[42:43], v[58:59], 0, v[42:43]
	global_store_dwordx4 v[54:55], v[46:49], off sc1
	global_store_dwordx4 v[42:43], v[38:41], off sc1
	s_or_b32 s6, s6, 1
	s_waitcnt lgkmcnt(0)
	v_cvt_f32_f16_e32 v42, v34
	v_cvt_f32_f16_sdwa v43, v34 dst_sel:DWORD dst_unused:UNUSED_PAD src0_sel:WORD_1
	v_cvt_f32_f16_e32 v34, v35
	v_cvt_f32_f16_sdwa v35, v35 dst_sel:DWORD dst_unused:UNUSED_PAD src0_sel:WORD_1
	s_ashr_i32 s7, s6, 31
	s_lshl_b64 s[6:7], s[6:7], 12
	v_pk_fma_f32 v[30:31], v[130:131], v[30:31], v[42:43] op_sel:[1,0,0]
	v_pk_fma_f32 v[32:33], v[130:131], v[32:33], v[34:35] op_sel:[1,0,0]
	v_cvt_f32_f16_e32 v34, v36
	v_cvt_f32_f16_sdwa v35, v36 dst_sel:DWORD dst_unused:UNUSED_PAD src0_sel:WORD_1
	v_cvt_f32_f16_e32 v36, v37
	v_cvt_f32_f16_sdwa v37, v37 dst_sel:DWORD dst_unused:UNUSED_PAD src0_sel:WORD_1
	s_add_u32 s6, s6, s10
	v_pk_fma_f32 v[26:27], v[130:131], v[26:27], v[34:35] op_sel:[1,0,0]
	v_cvt_pk_f16_f32 v30, v30, v31
	v_cvt_pk_f16_f32 v31, v32, v33
	v_cvt_pk_f16_f32 v32, v26, v27
	v_pk_fma_f32 v[26:27], v[130:131], v[28:29], v[36:37] op_sel:[1,0,0]
	s_addc_u32 s3, s7, s3
	v_cvt_pk_f16_f32 v33, v26, v27
	v_or_b32_e32 v26, s6, v1
	v_mov_b32_e32 v27, s3
	v_lshlrev_b64 v[28:29], 8, v[26:27]
	v_lshl_add_u64 v[28:29], v[58:59], 0, v[28:29]
	ds_read_b128 v[38:41], v83 offset:52224
	v_cvt_f32_f16_e32 v34, v74
	v_cvt_f32_f16_sdwa v35, v74 dst_sel:DWORD dst_unused:UNUSED_PAD src0_sel:WORD_1
	v_cvt_f32_f16_e32 v36, v75
	v_cvt_f32_f16_sdwa v37, v75 dst_sel:DWORD dst_unused:UNUSED_PAD src0_sel:WORD_1
	global_store_dwordx4 v[28:29], v[30:33], off sc1
	v_cvt_f32_f16_e32 v28, v76
	v_cvt_f32_f16_sdwa v29, v76 dst_sel:DWORD dst_unused:UNUSED_PAD src0_sel:WORD_1
	v_cvt_f32_f16_e32 v30, v77
	v_cvt_f32_f16_sdwa v31, v77 dst_sel:DWORD dst_unused:UNUSED_PAD src0_sel:WORD_1
	s_waitcnt vmcnt(7)
	v_pk_fma_f32 v[22:23], v[130:131], v[22:23], v[34:35] op_sel:[1,0,0]
	v_pk_fma_f32 v[24:25], v[130:131], v[24:25], v[36:37] op_sel:[1,0,0]
	v_pk_fma_f32 v[18:19], v[130:131], v[18:19], v[28:29] op_sel:[1,0,0]
	v_cvt_pk_f16_f32 v22, v22, v23
	v_cvt_pk_f16_f32 v23, v24, v25
	v_cvt_pk_f16_f32 v24, v18, v19
	v_pk_fma_f32 v[18:19], v[130:131], v[20:21], v[30:31] op_sel:[1,0,0]
	v_or_b32_e32 v26, s6, v137
	s_waitcnt lgkmcnt(0)
	v_cvt_f32_f16_e32 v20, v38
	v_cvt_f32_f16_sdwa v21, v38 dst_sel:DWORD dst_unused:UNUSED_PAD src0_sel:WORD_1
	v_cvt_pk_f16_f32 v25, v18, v19
	v_lshlrev_b64 v[18:19], 8, v[26:27]
	v_lshl_add_u64 v[18:19], v[58:59], 0, v[18:19]
	v_cvt_f32_f16_e32 v28, v39
	v_cvt_f32_f16_sdwa v29, v39 dst_sel:DWORD dst_unused:UNUSED_PAD src0_sel:WORD_1
	global_store_dwordx4 v[18:19], v[22:25], off sc1
	v_cvt_f32_f16_e32 v18, v40
	v_cvt_f32_f16_sdwa v19, v40 dst_sel:DWORD dst_unused:UNUSED_PAD src0_sel:WORD_1
	v_pk_fma_f32 v[14:15], v[130:131], v[14:15], v[20:21] op_sel:[1,0,0]
	v_cvt_f32_f16_e32 v20, v41
	v_cvt_f32_f16_sdwa v21, v41 dst_sel:DWORD dst_unused:UNUSED_PAD src0_sel:WORD_1
	v_pk_fma_f32 v[16:17], v[130:131], v[16:17], v[28:29] op_sel:[1,0,0]
	v_pk_fma_f32 v[10:11], v[130:131], v[10:11], v[18:19] op_sel:[1,0,0]
	v_cvt_pk_f16_f32 v14, v14, v15
	v_cvt_pk_f16_f32 v15, v16, v17
	v_cvt_pk_f16_f32 v16, v10, v11
	v_pk_fma_f32 v[10:11], v[130:131], v[12:13], v[20:21] op_sel:[1,0,0]
	v_or_b32_e32 v26, s6, v135
	v_cvt_f32_f16_e32 v12, v50
	v_cvt_f32_f16_sdwa v13, v50 dst_sel:DWORD dst_unused:UNUSED_PAD src0_sel:WORD_1
	v_cvt_pk_f16_f32 v17, v10, v11
	v_lshlrev_b64 v[10:11], 8, v[26:27]
	v_lshl_add_u64 v[10:11], v[58:59], 0, v[10:11]
	v_cvt_f32_f16_e32 v18, v51
	v_cvt_f32_f16_sdwa v19, v51 dst_sel:DWORD dst_unused:UNUSED_PAD src0_sel:WORD_1
	global_store_dwordx4 v[10:11], v[14:17], off sc1
	v_cvt_f32_f16_e32 v10, v52
	v_cvt_f32_f16_sdwa v11, v52 dst_sel:DWORD dst_unused:UNUSED_PAD src0_sel:WORD_1
	s_waitcnt vmcnt(7)
	v_pk_fma_f32 v[6:7], v[130:131], v[6:7], v[12:13] op_sel:[1,0,0]
	v_cvt_f32_f16_e32 v12, v53
	v_cvt_f32_f16_sdwa v13, v53 dst_sel:DWORD dst_unused:UNUSED_PAD src0_sel:WORD_1
	v_pk_fma_f32 v[8:9], v[130:131], v[8:9], v[18:19] op_sel:[1,0,0]
	v_pk_fma_f32 v[2:3], v[130:131], v[2:3], v[10:11] op_sel:[1,0,0]
	v_cvt_pk_f16_f32 v6, v6, v7
	v_cvt_pk_f16_f32 v7, v8, v9
	v_cvt_pk_f16_f32 v8, v2, v3
	v_pk_fma_f32 v[2:3], v[130:131], v[4:5], v[12:13] op_sel:[1,0,0]
	v_or_b32_e32 v26, s6, v136
	v_cvt_pk_f16_f32 v9, v2, v3
	v_lshlrev_b64 v[2:3], 8, v[26:27]
	v_lshl_add_u64 v[2:3], v[58:59], 0, v[2:3]
	global_store_dwordx4 v[2:3], v[6:9], off sc1
	s_branch .LBB2_2

.LBB2_24:
	s_or_b64 exec, exec, s[0:1]
	s_and_b32 s4, s20, 0x700000
	s_cmp_lt_u32 s3, 64
	s_cselect_b64 vcc, -1, 0
	s_and_b64 s[0:1], vcc, exec
	s_cselect_b32 s1, s13, s15
	s_cselect_b32 s0, s12, s14
	s_lshl_b32 s3, s4, 1
	v_mov_b32_e32 v137, 0x3e0293ee
	s_add_u32 s0, s0, s3
	v_cndmask_b32_e32 v158, 1.0, v137, vcc
	s_addc_u32 s1, s1, 0
	v_lshlrev_b32_e32 v136, 6, v136
	v_lshlrev_b32_e32 v137, 2, v130
	v_lshlrev_b32_e32 v130, 4, v130
	v_add3_u32 v162, 0, v136, v137
	v_add_u32_e32 v182, 0, v130
	v_lshl_add_u64 v[136:137], s[0:1], 0, v[130:131]
	v_lshrrev_b16_e32 v130, 2, v0
	v_lshlrev_b16_e32 v192, 6, v154
	v_and_b32_e32 v191, 12, v130
	v_bitop3_b16 v194, v192, v130, 12 bitop3:0xf8
	v_lshlrev_b32_e32 v130, 2, v187
	v_lshlrev_b32_e32 v189, 2, v189
	v_lshlrev_b32_e32 v188, 2, v188
	v_or_b32_e32 v154, v130, v1
	v_bitop3_b32 v130, v130, 1, v1 bitop3:0x36
	v_lshlrev_b32_e32 v190, 2, v190
	v_or_b32_e32 v195, v189, v1
	v_or_b32_e32 v196, v188, v1
	v_lshl_add_u32 v154, v154, 2, 0
	v_lshl_add_u32 v130, v130, 2, 0
	v_or_b32_e32 v193, v190, v1
	v_bitop3_b32 v190, v190, 1, v1 bitop3:0x36
	v_lshl_add_u32 v195, v195, 2, 0
	v_bitop3_b32 v189, v189, 1, v1 bitop3:0x36
	v_lshl_add_u32 v196, v196, 2, 0
	v_bitop3_b32 v188, v188, 1, v1 bitop3:0x36
	s_waitcnt lgkmcnt(0)
	s_barrier
	v_lshl_add_u32 v193, v193, 2, 0
	v_lshl_add_u32 v190, v190, 2, 0
	v_lshl_add_u32 v189, v189, 2, 0
	v_lshl_add_u32 v188, v188, 2, 0
	ds_read_b32 v154, v154
	ds_read_b32 v130, v130
	ds_read_b32 v197, v193
	ds_read_b32 v198, v190
	ds_read_b32 v195, v195
	ds_read_b32 v199, v189
	ds_read_b32 v196, v196
	ds_read_b32 v200, v188
	s_waitcnt lgkmcnt(6)
	v_add_f32_e32 v130, v154, v130
	v_bfrev_b32_e32 v154, 44
	v_fmamk_f32 v130, v130, 0x3c000000, v154
	v_rsq_f32_e32 v188, v130
	v_bitop3_b16 v201, v192, 16, v191 bitop3:0xfe
	v_bitop3_b16 v202, v192, 32, v191 bitop3:0xfe
	v_bitop3_b16 v130, v192, 48, v191 bitop3:0xfe
	v_mul_f32_e32 v188, v158, v188
	v_mov_b32_e32 v190, v118
	v_mov_b32_e32 v191, v114
	v_mov_b32_e32 v192, v122
	v_mov_b32_e32 v193, v126
	v_pk_mul_f32 v[190:191], v[190:191], v[188:189] op_sel_hi:[1,0]
	v_pk_mul_f32 v[188:189], v[192:193], v[188:189] op_sel_hi:[1,0]
	v_and_b32_e32 v161, 0x80, v0
	s_movk_i32 s1, 0x4c
	s_waitcnt vmcnt(6)
	v_pk_mul_f32 v[192:193], v[144:145], v[188:189]
	s_movk_i32 s0, 0x110
	v_and_or_b32 v187, v187, s1, v161
	v_pk_fma_f32 v[192:193], v[142:143], v[190:191], v[192:193]
	v_pk_mul_f32 v[190:191], v[144:145], v[190:191]
	v_mad_u32_u24 v187, v187, s0, v162
	v_pk_fma_f32 v[188:189], v[142:143], v[188:189], v[190:191] neg_lo:[0,0,1] neg_hi:[0,0,1]
	v_cvt_pk_f16_f32 v114, v192, v193
	v_cvt_pk_f16_f32 v122, v188, v189
	v_add_u32_e32 v118, 0x1000, v187
	ds_write2_b32 v118, v114, v122 offset1:32
	s_waitcnt lgkmcnt(5)
	v_add_f32_e32 v114, v197, v198
	v_fmamk_f32 v114, v114, 0x3c000000, v154
	v_rsq_f32_e32 v114, v114
	s_waitcnt vmcnt(4)
	v_pk_mul_f32 v[190:191], v[142:143], v[134:135]
	v_mov_b32_e32 v126, v123
	v_pk_mul_f32 v[188:189], v[144:145], v[134:135]
	v_mul_f32_e32 v122, v158, v114
	v_or_b32_sdwa v114, v161, v194 dst_sel:DWORD dst_unused:UNUSED_PAD src0_sel:DWORD src1_sel:WORD_0
	v_mad_u32_u24 v187, v114, s0, v162
	v_mov_b32_e32 v114, v119
	v_pk_fma_f32 v[190:191], v[144:145], v[132:133], v[190:191]
	v_pk_mul_f32 v[114:115], v[114:115], v[122:123] op_sel_hi:[1,0]
	v_pk_mul_f32 v[122:123], v[126:127], v[122:123] op_sel_hi:[1,0]
	v_pk_fma_f32 v[188:189], v[142:143], v[132:133], v[188:189] neg_lo:[0,0,1] neg_hi:[0,0,1]
	v_pk_mul_f32 v[126:127], v[190:191], v[122:123]
	v_mov_b32_e32 v192, v124
	v_pk_fma_f32 v[126:127], v[188:189], v[114:115], v[126:127]
	v_pk_mul_f32 v[114:115], v[190:191], v[114:115]
	v_cvt_pk_f16_f32 v119, v126, v127
	v_pk_fma_f32 v[114:115], v[188:189], v[122:123], v[114:115] neg_lo:[0,0,1] neg_hi:[0,0,1]
	v_pk_mul_f32 v[122:123], v[134:135], v[190:191]
	v_cvt_pk_f16_f32 v115, v114, v115
	v_add_u32_e32 v114, 0x1000, v187
	ds_write2_b32 v114, v119, v115 offset0:68 offset1:100
	s_waitcnt lgkmcnt(4)
	v_add_f32_e32 v115, v195, v199
	v_fmamk_f32 v115, v115, 0x3c000000, v154
	v_rsq_f32_e32 v115, v115
	v_pk_mul_f32 v[126:127], v[132:133], v[190:191]
	v_pk_fma_f32 v[122:123], v[132:133], v[188:189], v[122:123] neg_lo:[0,0,1] neg_hi:[0,0,1]
	v_pk_fma_f32 v[126:127], v[134:135], v[188:189], v[126:127]
	v_mul_f32_e32 v188, v158, v115
	v_mov_b32_e32 v190, v120
	v_mov_b32_e32 v191, v116
	v_mov_b32_e32 v193, v128
	v_pk_mul_f32 v[190:191], v[190:191], v[188:189] op_sel_hi:[1,0]
	v_pk_mul_f32 v[188:189], v[192:193], v[188:189] op_sel_hi:[1,0]
	v_mov_b32_e32 v128, v125
	v_pk_mul_f32 v[192:193], v[126:127], v[188:189]
	s_movk_i32 s1, 0x5c
	v_pk_fma_f32 v[192:193], v[122:123], v[190:191], v[192:193]
	v_pk_mul_f32 v[190:191], v[126:127], v[190:191]
	v_cvt_pk_f16_f32 v115, v192, v193
	v_pk_fma_f32 v[188:189], v[122:123], v[188:189], v[190:191] neg_lo:[0,0,1] neg_hi:[0,0,1]
	s_movk_i32 s3, 0x6c
	v_cvt_pk_f16_f32 v116, v188, v189
	ds_write2_b32 v114, v115, v116 offset0:136 offset1:168
	s_waitcnt lgkmcnt(3)
	v_add_f32_e32 v115, v196, v200
	v_fmamk_f32 v115, v115, 0x3c000000, v154
	v_rsq_f32_e32 v115, v115
	v_pk_mul_f32 v[188:189], v[134:135], v[126:127]
	v_pk_mul_f32 v[126:127], v[132:133], v[126:127]
	v_mov_b32_e32 v116, v121
	v_mul_f32_e32 v120, v158, v115
	v_pk_fma_f32 v[188:189], v[132:133], v[122:123], v[188:189] neg_lo:[0,0,1] neg_hi:[0,0,1]
	v_pk_fma_f32 v[122:123], v[134:135], v[122:123], v[126:127]
	v_pk_mul_f32 v[116:117], v[116:117], v[120:121] op_sel_hi:[1,0]
	v_pk_mul_f32 v[120:121], v[128:129], v[120:121] op_sel_hi:[1,0]
	v_mov_b32_e32 v126, v106
	v_pk_mul_f32 v[124:125], v[122:123], v[120:121]
	v_mov_b32_e32 v127, v110
	v_pk_fma_f32 v[124:125], v[188:189], v[116:117], v[124:125]
	v_pk_mul_f32 v[116:117], v[122:123], v[116:117]
	v_cvt_pk_f16_f32 v115, v124, v125
	v_pk_fma_f32 v[116:117], v[188:189], v[120:121], v[116:117] neg_lo:[0,0,1] neg_hi:[0,0,1]
	v_lshlrev_b32_e32 v120, 2, v186
	v_cvt_pk_f16_f32 v116, v116, v117
	ds_write2_b32 v114, v115, v116 offset0:204 offset1:236
	v_lshlrev_b32_e32 v115, 2, v183
	v_or_b32_e32 v119, v115, v1
	v_bitop3_b32 v115, v115, 1, v1 bitop3:0x36
	v_lshlrev_b32_e32 v122, 2, v185
	v_lshlrev_b32_e32 v124, 2, v184
	v_lshl_add_u32 v119, v119, 2, 0
	v_lshl_add_u32 v115, v115, 2, 0
	v_or_b32_e32 v121, v120, v1
	v_bitop3_b32 v120, v120, 1, v1 bitop3:0x36
	v_or_b32_e32 v123, v122, v1
	v_bitop3_b32 v122, v122, 1, v1 bitop3:0x36
	v_or_b32_e32 v125, v124, v1
	v_bitop3_b32 v124, v124, 1, v1 bitop3:0x36
	v_lshl_add_u32 v121, v121, 2, 0
	v_lshl_add_u32 v120, v120, 2, 0
	v_lshl_add_u32 v123, v123, 2, 0
	v_lshl_add_u32 v122, v122, 2, 0
	v_lshl_add_u32 v125, v125, 2, 0
	v_lshl_add_u32 v124, v124, 2, 0
	ds_read_b32 v119, v119
	ds_read_b32 v115, v115
	ds_read_b32 v128, v121
	ds_read_b32 v129, v120
	ds_read_b32 v184, v123
	ds_read_b32 v185, v122
	ds_read_b32 v186, v125
	ds_read_b32 v187, v124
	s_waitcnt lgkmcnt(6)
	v_add_f32_e32 v115, v119, v115
	v_fmamk_f32 v115, v115, 0x3c000000, v154
	v_rsq_f32_e32 v115, v115
	s_waitcnt vmcnt(2)
	v_pk_mul_f32 v[120:121], v[142:143], v[140:141]
	v_mov_b32_e32 v124, v102
	v_mov_b32_e32 v125, v98
	v_mul_f32_e32 v122, v158, v115
	v_pk_mul_f32 v[116:117], v[144:145], v[140:141]
	v_pk_fma_f32 v[120:121], v[144:145], v[138:139], v[120:121]
	v_pk_mul_f32 v[124:125], v[124:125], v[122:123] op_sel_hi:[1,0]
	v_pk_mul_f32 v[122:123], v[126:127], v[122:123] op_sel_hi:[1,0]
	v_pk_fma_f32 v[116:117], v[142:143], v[138:139], v[116:117] neg_lo:[0,0,1] neg_hi:[0,0,1]
	v_pk_mul_f32 v[126:127], v[120:121], v[122:123]
	v_and_or_b32 v115, v183, s1, v161
	v_pk_fma_f32 v[126:127], v[116:117], v[124:125], v[126:127]
	v_pk_mul_f32 v[124:125], v[120:121], v[124:125]
	v_mad_u32_u24 v115, v115, s0, v162
	v_pk_fma_f32 v[122:123], v[116:117], v[122:123], v[124:125] neg_lo:[0,0,1] neg_hi:[0,0,1]
	v_cvt_pk_f16_f32 v98, v126, v127
	v_cvt_pk_f16_f32 v102, v122, v123
	v_add_u32_e32 v106, 0x1000, v115
	ds_write2_b32 v106, v98, v102 offset1:32
	s_waitcnt lgkmcnt(5)
	v_add_f32_e32 v98, v128, v129
	v_fmamk_f32 v98, v98, 0x3c000000, v154
	v_rsq_f32_e32 v98, v98
	v_pk_mul_f32 v[124:125], v[132:133], v[120:121]
	v_mov_b32_e32 v110, v107
	v_pk_mul_f32 v[122:123], v[134:135], v[120:121]
	v_mul_f32_e32 v102, v158, v98
	v_or_b32_sdwa v98, v161, v201 dst_sel:DWORD dst_unused:UNUSED_PAD src0_sel:DWORD src1_sel:WORD_0
	v_mad_u32_u24 v115, v98, s0, v162
	v_mov_b32_e32 v98, v103
	v_pk_fma_f32 v[124:125], v[134:135], v[116:117], v[124:125]
	v_pk_mul_f32 v[98:99], v[98:99], v[102:103] op_sel_hi:[1,0]
	v_pk_mul_f32 v[102:103], v[110:111], v[102:103] op_sel_hi:[1,0]
	v_pk_fma_f32 v[122:123], v[132:133], v[116:117], v[122:123] neg_lo:[0,0,1] neg_hi:[0,0,1]
	v_pk_mul_f32 v[106:107], v[124:125], v[102:103]
	s_movk_i32 s4, 0x7c
	v_pk_fma_f32 v[106:107], v[122:123], v[98:99], v[106:107]
	v_pk_mul_f32 v[98:99], v[124:125], v[98:99]
	v_cvt_pk_f16_f32 v106, v106, v107
	v_pk_fma_f32 v[98:99], v[122:123], v[102:103], v[98:99] neg_lo:[0,0,1] neg_hi:[0,0,1]
	v_pk_mul_f32 v[102:103], v[134:135], v[124:125]
	v_cvt_pk_f16_f32 v99, v98, v99
	v_add_u32_e32 v98, 0x1000, v115
	ds_write2_b32 v98, v106, v99 offset0:68 offset1:100
	s_waitcnt lgkmcnt(4)
	v_add_f32_e32 v99, v184, v185
	v_fmamk_f32 v99, v99, 0x3c000000, v154
	v_rsq_f32_e32 v99, v99
	v_pk_mul_f32 v[106:107], v[132:133], v[124:125]
	v_pk_fma_f32 v[102:103], v[132:133], v[122:123], v[102:103] neg_lo:[0,0,1] neg_hi:[0,0,1]
	v_pk_fma_f32 v[106:107], v[134:135], v[122:123], v[106:107]
	v_mul_f32_e32 v110, v158, v99
	v_mov_b32_e32 v122, v104
	v_mov_b32_e32 v123, v100
	v_mov_b32_e32 v124, v108
	v_mov_b32_e32 v125, v112
	v_pk_mul_f32 v[122:123], v[122:123], v[110:111] op_sel_hi:[1,0]
	v_pk_mul_f32 v[110:111], v[124:125], v[110:111] op_sel_hi:[1,0]
	v_mov_b32_e32 v112, v109
	v_pk_mul_f32 v[124:125], v[106:107], v[110:111]
	v_mov_b32_e32 v109, v94
	v_pk_fma_f32 v[124:125], v[102:103], v[122:123], v[124:125]
	v_pk_mul_f32 v[122:123], v[106:107], v[122:123]
	v_cvt_pk_f16_f32 v99, v124, v125
	v_pk_fma_f32 v[110:111], v[102:103], v[110:111], v[122:123] neg_lo:[0,0,1] neg_hi:[0,0,1]
	v_mov_b32_e32 v94, v91
	v_cvt_pk_f16_f32 v100, v110, v111
	ds_write2_b32 v98, v99, v100 offset0:136 offset1:168
	s_waitcnt lgkmcnt(3)
	v_add_f32_e32 v99, v186, v187
	v_fmamk_f32 v99, v99, 0x3c000000, v154
	v_rsq_f32_e32 v99, v99
	v_pk_mul_f32 v[110:111], v[134:135], v[106:107]
	v_pk_mul_f32 v[106:107], v[132:133], v[106:107]
	v_mov_b32_e32 v100, v105
	v_mul_f32_e32 v104, v158, v99
	v_pk_fma_f32 v[110:111], v[132:133], v[102:103], v[110:111] neg_lo:[0,0,1] neg_hi:[0,0,1]
	v_pk_fma_f32 v[102:103], v[134:135], v[102:103], v[106:107]
	v_pk_mul_f32 v[100:101], v[100:101], v[104:105] op_sel_hi:[1,0]
	v_pk_mul_f32 v[104:105], v[112:113], v[104:105] op_sel_hi:[1,0]
	v_mad_u32_u24 v155, v152, s0, v182
	v_pk_mul_f32 v[106:107], v[102:103], v[104:105]
	s_or_b32 s5, s2, 0x1000
	v_pk_fma_f32 v[106:107], v[110:111], v[100:101], v[106:107]
	v_pk_mul_f32 v[100:101], v[102:103], v[100:101]
	v_cvt_pk_f16_f32 v99, v106, v107
	v_pk_fma_f32 v[100:101], v[110:111], v[104:105], v[100:101] neg_lo:[0,0,1] neg_hi:[0,0,1]
	v_lshlrev_b32_e32 v103, 2, v181
	v_cvt_pk_f16_f32 v100, v100, v101
	ds_write2_b32 v98, v99, v100 offset0:204 offset1:236
	v_lshlrev_b32_e32 v99, 2, v178
	v_or_b32_e32 v102, v99, v1
	v_bitop3_b32 v99, v99, 1, v1 bitop3:0x36
	v_lshlrev_b32_e32 v105, 2, v180
	v_lshlrev_b32_e32 v107, 2, v179
	v_lshl_add_u32 v102, v102, 2, 0
	v_lshl_add_u32 v99, v99, 2, 0
	v_or_b32_e32 v104, v103, v1
	v_bitop3_b32 v103, v103, 1, v1 bitop3:0x36
	v_or_b32_e32 v106, v105, v1
	v_bitop3_b32 v105, v105, 1, v1 bitop3:0x36
	v_or_b32_e32 v108, v107, v1
	v_bitop3_b32 v107, v107, 1, v1 bitop3:0x36
	v_lshl_add_u32 v104, v104, 2, 0
	v_lshl_add_u32 v103, v103, 2, 0
	v_lshl_add_u32 v106, v106, 2, 0
	v_lshl_add_u32 v105, v105, 2, 0
	v_lshl_add_u32 v108, v108, 2, 0
	v_lshl_add_u32 v107, v107, 2, 0
	ds_read_b32 v102, v102
	ds_read_b32 v99, v99
	ds_read_b32 v110, v104
	ds_read_b32 v111, v103
	ds_read_b32 v112, v106
	ds_read_b32 v113, v105
	ds_read_b32 v115, v108
	ds_read_b32 v119, v107
	s_waitcnt lgkmcnt(6)
	v_add_f32_e32 v99, v102, v99
	v_fmamk_f32 v99, v99, 0x3c000000, v154
	v_rsq_f32_e32 v99, v99
	v_pk_mul_f32 v[102:103], v[138:139], v[120:121]
	v_mov_b32_e32 v106, v86
	v_mov_b32_e32 v107, v82
	v_mul_f32_e32 v104, v158, v99
	v_mov_b32_e32 v108, v90
	v_pk_mul_f32 v[100:101], v[140:141], v[120:121]
	v_pk_fma_f32 v[102:103], v[140:141], v[116:117], v[102:103]
	v_pk_mul_f32 v[106:107], v[106:107], v[104:105] op_sel_hi:[1,0]
	v_pk_mul_f32 v[104:105], v[108:109], v[104:105] op_sel_hi:[1,0]
	v_pk_fma_f32 v[100:101], v[138:139], v[116:117], v[100:101] neg_lo:[0,0,1] neg_hi:[0,0,1]
	v_pk_mul_f32 v[108:109], v[102:103], v[104:105]
	v_and_or_b32 v99, v178, s3, v161
	v_pk_fma_f32 v[108:109], v[100:101], v[106:107], v[108:109]
	v_pk_mul_f32 v[106:107], v[102:103], v[106:107]
	v_mad_u32_u24 v99, v99, s0, v162
	v_pk_fma_f32 v[104:105], v[100:101], v[104:105], v[106:107] neg_lo:[0,0,1] neg_hi:[0,0,1]
	v_cvt_pk_f16_f32 v82, v108, v109
	v_cvt_pk_f16_f32 v86, v104, v105
	v_add_u32_e32 v90, 0x1000, v99
	ds_write2_b32 v90, v82, v86 offset1:32
	s_waitcnt lgkmcnt(5)
	v_add_f32_e32 v82, v110, v111
	v_fmamk_f32 v82, v82, 0x3c000000, v154
	v_rsq_f32_e32 v82, v82
	v_pk_mul_f32 v[106:107], v[132:133], v[102:103]
	v_pk_mul_f32 v[104:105], v[134:135], v[102:103]
	v_pk_fma_f32 v[106:107], v[134:135], v[100:101], v[106:107]
	v_mul_f32_e32 v86, v158, v82
	v_or_b32_sdwa v82, v161, v202 dst_sel:DWORD dst_unused:UNUSED_PAD src0_sel:DWORD src1_sel:WORD_0
	v_mad_u32_u24 v99, v82, s0, v162
	v_mov_b32_e32 v82, v87
	v_pk_mul_f32 v[82:83], v[82:83], v[86:87] op_sel_hi:[1,0]
	v_pk_mul_f32 v[86:87], v[94:95], v[86:87] op_sel_hi:[1,0]
	v_pk_fma_f32 v[104:105], v[132:133], v[100:101], v[104:105] neg_lo:[0,0,1] neg_hi:[0,0,1]
	v_pk_mul_f32 v[90:91], v[106:107], v[86:87]
	s_waitcnt vmcnt(0)
	v_pk_mul_f32 v[150:151], v[144:145], v[148:149]
	v_pk_fma_f32 v[90:91], v[104:105], v[82:83], v[90:91]
	v_pk_mul_f32 v[82:83], v[106:107], v[82:83]
	v_cvt_pk_f16_f32 v90, v90, v91
	v_pk_fma_f32 v[82:83], v[104:105], v[86:87], v[82:83] neg_lo:[0,0,1] neg_hi:[0,0,1]
	v_pk_mul_f32 v[86:87], v[134:135], v[106:107]
	v_cvt_pk_f16_f32 v83, v82, v83
	v_add_u32_e32 v82, 0x1000, v99
	ds_write2_b32 v82, v90, v83 offset0:68 offset1:100
	s_waitcnt lgkmcnt(4)
	v_add_f32_e32 v83, v112, v113
	v_fmamk_f32 v83, v83, 0x3c000000, v154
	v_rsq_f32_e32 v83, v83
	v_pk_mul_f32 v[90:91], v[132:133], v[106:107]
	v_pk_fma_f32 v[86:87], v[132:133], v[104:105], v[86:87] neg_lo:[0,0,1] neg_hi:[0,0,1]
	v_pk_fma_f32 v[90:91], v[134:135], v[104:105], v[90:91]
	v_mul_f32_e32 v94, v158, v83
	v_mov_b32_e32 v104, v88
	v_mov_b32_e32 v105, v84
	v_mov_b32_e32 v106, v92
	v_mov_b32_e32 v107, v96
	v_pk_mul_f32 v[104:105], v[104:105], v[94:95] op_sel_hi:[1,0]
	v_pk_mul_f32 v[94:95], v[106:107], v[94:95] op_sel_hi:[1,0]
	v_mov_b32_e32 v96, v93
	v_pk_mul_f32 v[106:107], v[90:91], v[94:95]
	v_mov_b32_e32 v93, v78
	v_pk_fma_f32 v[106:107], v[86:87], v[104:105], v[106:107]
	v_pk_mul_f32 v[104:105], v[90:91], v[104:105]
	v_cvt_pk_f16_f32 v83, v106, v107
	v_pk_fma_f32 v[94:95], v[86:87], v[94:95], v[104:105] neg_lo:[0,0,1] neg_hi:[0,0,1]
	v_mov_b32_e32 v78, v75
	v_cvt_pk_f16_f32 v84, v94, v95
	ds_write2_b32 v82, v83, v84 offset0:136 offset1:168
	s_waitcnt lgkmcnt(3)
	v_add_f32_e32 v83, v115, v119
	v_fmamk_f32 v83, v83, 0x3c000000, v154
	v_rsq_f32_e32 v83, v83
	v_pk_mul_f32 v[94:95], v[134:135], v[90:91]
	v_pk_mul_f32 v[90:91], v[132:133], v[90:91]
	v_mov_b32_e32 v84, v89
	v_mul_f32_e32 v88, v158, v83
	v_pk_fma_f32 v[94:95], v[132:133], v[86:87], v[94:95] neg_lo:[0,0,1] neg_hi:[0,0,1]
	v_pk_fma_f32 v[86:87], v[134:135], v[86:87], v[90:91]
	v_pk_mul_f32 v[84:85], v[84:85], v[88:89] op_sel_hi:[1,0]
	v_pk_mul_f32 v[88:89], v[96:97], v[88:89] op_sel_hi:[1,0]
	s_nop 0
	v_pk_mul_f32 v[90:91], v[86:87], v[88:89]
	s_nop 0
	v_pk_fma_f32 v[90:91], v[94:95], v[84:85], v[90:91]
	v_pk_mul_f32 v[84:85], v[86:87], v[84:85]
	v_cvt_pk_f16_f32 v83, v90, v91
	v_pk_fma_f32 v[84:85], v[94:95], v[88:89], v[84:85] neg_lo:[0,0,1] neg_hi:[0,0,1]
	v_lshlrev_b32_e32 v87, 2, v177
	v_cvt_pk_f16_f32 v84, v84, v85
	ds_write2_b32 v82, v83, v84 offset0:204 offset1:236
	v_lshlrev_b32_e32 v83, 2, v174
	v_or_b32_e32 v86, v83, v1
	v_bitop3_b32 v83, v83, 1, v1 bitop3:0x36
	v_lshlrev_b32_e32 v89, 2, v176
	v_lshlrev_b32_e32 v91, 2, v175
	v_lshl_add_u32 v86, v86, 2, 0
	v_lshl_add_u32 v83, v83, 2, 0
	v_or_b32_e32 v88, v87, v1
	v_bitop3_b32 v87, v87, 1, v1 bitop3:0x36
	v_or_b32_e32 v90, v89, v1
	v_bitop3_b32 v89, v89, 1, v1 bitop3:0x36
	v_or_b32_e32 v92, v91, v1
	v_bitop3_b32 v91, v91, 1, v1 bitop3:0x36
	v_lshl_add_u32 v88, v88, 2, 0
	v_lshl_add_u32 v87, v87, 2, 0
	v_lshl_add_u32 v90, v90, 2, 0
	v_lshl_add_u32 v89, v89, 2, 0
	v_lshl_add_u32 v92, v92, 2, 0
	v_lshl_add_u32 v91, v91, 2, 0
	ds_read_b32 v86, v86
	ds_read_b32 v83, v83
	ds_read_b32 v94, v88
	ds_read_b32 v95, v87
	ds_read_b32 v96, v90
	ds_read_b32 v97, v89
	ds_read_b32 v99, v92
	ds_read_b32 v104, v91
	s_waitcnt lgkmcnt(6)
	v_add_f32_e32 v83, v86, v83
	v_fmamk_f32 v83, v83, 0x3c000000, v154
	v_rsq_f32_e32 v83, v83
	v_pk_mul_f32 v[86:87], v[138:139], v[102:103]
	v_mov_b32_e32 v90, v70
	v_mov_b32_e32 v91, v66
	v_mul_f32_e32 v88, v158, v83
	v_mov_b32_e32 v92, v74
	v_pk_mul_f32 v[84:85], v[140:141], v[102:103]
	v_pk_fma_f32 v[86:87], v[140:141], v[100:101], v[86:87]
	v_pk_mul_f32 v[90:91], v[90:91], v[88:89] op_sel_hi:[1,0]
	v_pk_mul_f32 v[88:89], v[92:93], v[88:89] op_sel_hi:[1,0]
	v_pk_fma_f32 v[84:85], v[138:139], v[100:101], v[84:85] neg_lo:[0,0,1] neg_hi:[0,0,1]
	v_pk_mul_f32 v[92:93], v[86:87], v[88:89]
	v_and_or_b32 v83, v174, s4, v161
	v_pk_fma_f32 v[92:93], v[84:85], v[90:91], v[92:93]
	v_pk_mul_f32 v[90:91], v[86:87], v[90:91]
	v_mad_u32_u24 v83, v83, s0, v162
	v_pk_fma_f32 v[88:89], v[84:85], v[88:89], v[90:91] neg_lo:[0,0,1] neg_hi:[0,0,1]
	v_cvt_pk_f16_f32 v66, v92, v93
	v_cvt_pk_f16_f32 v70, v88, v89
	v_add_u32_e32 v74, 0x1000, v83
	ds_write2_b32 v74, v66, v70 offset1:32
	s_waitcnt lgkmcnt(5)
	v_add_f32_e32 v66, v94, v95
	v_fmamk_f32 v66, v66, 0x3c000000, v154
	v_rsq_f32_e32 v66, v66
	v_pk_mul_f32 v[88:89], v[134:135], v[86:87]
	v_pk_mul_f32 v[86:87], v[132:133], v[86:87]
	v_pk_fma_f32 v[88:89], v[132:133], v[84:85], v[88:89] neg_lo:[0,0,1] neg_hi:[0,0,1]
	v_mul_f32_e32 v70, v158, v66
	v_or_b32_sdwa v66, v161, v130 dst_sel:DWORD dst_unused:UNUSED_PAD src0_sel:DWORD src1_sel:WORD_0
	v_mad_u32_u24 v83, v66, s0, v162
	v_mov_b32_e32 v66, v71
	v_pk_fma_f32 v[84:85], v[134:135], v[84:85], v[86:87]
	v_pk_mul_f32 v[66:67], v[66:67], v[70:71] op_sel_hi:[1,0]
	v_pk_mul_f32 v[70:71], v[78:79], v[70:71] op_sel_hi:[1,0]
	v_mov_b32_e32 v78, v72
	v_pk_mul_f32 v[74:75], v[84:85], v[70:71]
	v_mov_b32_e32 v79, v68
	v_pk_fma_f32 v[74:75], v[88:89], v[66:67], v[74:75]
	v_pk_mul_f32 v[66:67], v[84:85], v[66:67]
	v_cvt_pk_f16_f32 v74, v74, v75
	v_pk_fma_f32 v[66:67], v[88:89], v[70:71], v[66:67] neg_lo:[0,0,1] neg_hi:[0,0,1]
	v_pk_mul_f32 v[70:71], v[134:135], v[84:85]
	v_cvt_pk_f16_f32 v66, v66, v67
	v_add_u32_e32 v67, 0x1000, v83
	ds_write2_b32 v67, v74, v66 offset0:68 offset1:100
	s_waitcnt lgkmcnt(4)
	v_add_f32_e32 v66, v96, v97
	v_fmamk_f32 v66, v66, 0x3c000000, v154
	v_rsq_f32_e32 v66, v66
	v_pk_mul_f32 v[74:75], v[132:133], v[84:85]
	v_mov_b32_e32 v84, v76
	v_mov_b32_e32 v85, v80
	v_mul_f32_e32 v66, v158, v66
	v_pk_fma_f32 v[74:75], v[134:135], v[88:89], v[74:75]
	v_pk_mul_f32 v[84:85], v[84:85], v[66:67] op_sel_hi:[1,0]
	v_pk_fma_f32 v[70:71], v[132:133], v[88:89], v[70:71] neg_lo:[0,0,1] neg_hi:[0,0,1]
	v_pk_mul_f32 v[78:79], v[78:79], v[66:67] op_sel_hi:[1,0]
	v_pk_mul_f32 v[86:87], v[74:75], v[84:85]
	v_mov_b32_e32 v80, v77
	v_pk_fma_f32 v[86:87], v[70:71], v[78:79], v[86:87]
	v_pk_mul_f32 v[78:79], v[74:75], v[78:79]
	v_cvt_pk_f16_f32 v66, v86, v87
	v_pk_fma_f32 v[78:79], v[70:71], v[84:85], v[78:79] neg_lo:[0,0,1] neg_hi:[0,0,1]
	s_nop 0
	v_cvt_pk_f16_f32 v68, v78, v79
	ds_write2_b32 v67, v66, v68 offset0:136 offset1:168
	s_waitcnt lgkmcnt(3)
	v_add_f32_e32 v66, v99, v104
	v_fmamk_f32 v66, v66, 0x3c000000, v154
	v_rsq_f32_e32 v66, v66
	v_pk_mul_f32 v[78:79], v[134:135], v[74:75]
	v_pk_mul_f32 v[74:75], v[132:133], v[74:75]
	v_pk_fma_f32 v[78:79], v[132:133], v[70:71], v[78:79] neg_lo:[0,0,1] neg_hi:[0,0,1]
	v_mul_f32_e32 v66, v158, v66
	v_pk_fma_f32 v[70:71], v[134:135], v[70:71], v[74:75]
	v_mov_b32_e32 v68, v73
	v_pk_mul_f32 v[72:73], v[80:81], v[66:67] op_sel_hi:[1,0]
	v_pk_mul_f32 v[68:69], v[68:69], v[66:67] op_sel_hi:[1,0]
	v_pk_mul_f32 v[74:75], v[70:71], v[72:73]
	s_nop 0
	v_pk_fma_f32 v[74:75], v[78:79], v[68:69], v[74:75]
	v_pk_mul_f32 v[68:69], v[70:71], v[68:69]
	v_cvt_pk_f16_f32 v66, v74, v75
	v_pk_fma_f32 v[68:69], v[78:79], v[72:73], v[68:69] neg_lo:[0,0,1] neg_hi:[0,0,1]
	s_nop 0
	v_cvt_pk_f16_f32 v68, v68, v69
	ds_write2_b32 v67, v66, v68 offset0:204 offset1:236
	s_waitcnt lgkmcnt(0)
	s_barrier
	ds_read_b128 v[70:73], v155 offset:4096
	v_or_b32_e32 v66, s2, v152
	v_lshlrev_b32_e32 v130, 8, v66
	v_or_b32_e32 v66, 0x200, v0
	v_lshrrev_b32_e32 v66, 4, v66
	v_lshl_add_u64 v[78:79], v[136:137], 0, v[130:131]
	v_mad_u32_u24 v68, v66, s0, v182
	v_or_b32_e32 v69, s2, v66
	ds_read_b128 v[74:77], v68 offset:38912
	s_waitcnt lgkmcnt(1)
	global_store_dwordx4 v[78:79], v[70:73], off sc1
	ds_read_b128 v[78:81], v68 offset:4096
	v_lshlrev_b32_e32 v130, 8, v69
	v_or_b32_e32 v69, 64, v152
	v_mad_u32_u24 v70, v69, s0, v182
	ds_read_b128 v[84:87], v70 offset:4096
	v_or_b32_e32 v0, 0x600, v0
	v_or_b32_e32 v71, s2, v69
	v_lshrrev_b32_e32 v0, 4, v0
	v_lshl_add_u64 v[72:73], v[136:137], 0, v[130:131]
	v_lshlrev_b32_e32 v130, 8, v71
	v_mad_u32_u24 v71, v0, s0, v182
	s_waitcnt lgkmcnt(1)
	global_store_dwordx4 v[72:73], v[78:81], off sc1
	ds_read_b128 v[78:81], v71 offset:4096
	v_lshl_add_u64 v[72:73], v[136:137], 0, v[130:131]
	s_waitcnt lgkmcnt(1)
	global_store_dwordx4 v[72:73], v[84:87], off sc1
	v_or_b32_e32 v72, s2, v0
	v_lshlrev_b32_e32 v130, 8, v72
	v_or_b32_e32 v72, 0x80, v0
	v_lshl_add_u64 v[88:89], v[136:137], 0, v[130:131]
	v_mad_u32_u24 v72, v72, s0, v182
	ds_read_b128 v[84:87], v72 offset:4096
	s_waitcnt lgkmcnt(1)
	global_store_dwordx4 v[88:89], v[78:81], off sc1
	ds_read_b128 v[78:81], v155 offset:38912
	v_or_b32_e32 v73, s5, v152
	ds_read_b128 v[88:91], v155 offset:56320
	v_lshlrev_b32_e32 v130, 8, v73
	v_or_b32_e32 v73, s5, v66
	v_lshl_add_u64 v[92:93], v[136:137], 0, v[130:131]
	v_lshlrev_b32_e32 v130, 8, v73
	v_or_b32_e32 v73, s5, v69
	s_waitcnt lgkmcnt(1)
	global_store_dwordx4 v[92:93], v[78:81], off sc1
	s_nop 1
	v_lshl_add_u64 v[78:79], v[136:137], 0, v[130:131]
	v_lshlrev_b32_e32 v130, 8, v73
	v_or_b32_e32 v73, s5, v0
	global_store_dwordx4 v[78:79], v[74:77], off sc1
	v_lshlrev_b32_e32 v79, 2, v170
	v_or_b32_e32 v80, v79, v1
	v_lshl_add_u64 v[74:75], v[136:137], 0, v[130:131]
	v_lshlrev_b32_e32 v130, 8, v73
	s_waitcnt lgkmcnt(0)
	global_store_dwordx4 v[74:75], v[88:91], off sc1
	v_lshl_add_u64 v[74:75], v[136:137], 0, v[130:131]
	v_lshlrev_b32_e32 v73, 2, v173
	global_store_dwordx4 v[74:75], v[84:87], off sc1
	v_or_b32_e32 v74, v73, v1
	v_bitop3_b32 v73, v73, 1, v1 bitop3:0x36
	v_lshlrev_b32_e32 v75, 2, v172
	v_lshlrev_b32_e32 v77, 2, v171
	v_lshl_add_u32 v74, v74, 2, 0
	v_lshl_add_u32 v73, v73, 2, 0
	v_or_b32_e32 v76, v75, v1
	v_bitop3_b32 v75, v75, 1, v1 bitop3:0x36
	v_or_b32_e32 v78, v77, v1
	v_bitop3_b32 v77, v77, 1, v1 bitop3:0x36
	v_bitop3_b32 v79, v79, 1, v1 bitop3:0x36
	s_barrier
	v_lshl_add_u32 v76, v76, 2, 0
	v_lshl_add_u32 v75, v75, 2, 0
	v_lshl_add_u32 v78, v78, 2, 0
	v_lshl_add_u32 v77, v77, 2, 0
	v_lshl_add_u32 v80, v80, 2, 0
	v_lshl_add_u32 v79, v79, 2, 0
	ds_read_b32 v74, v74
	ds_read_b32 v73, v73
	ds_read_b32 v83, v76
	ds_read_b32 v86, v75
	ds_read_b32 v87, v78
	ds_read_b32 v88, v77
	ds_read_b32 v89, v80
	ds_read_b32 v90, v79
	s_waitcnt lgkmcnt(6)
	v_add_f32_e32 v73, v74, v73
	v_fmamk_f32 v73, v73, 0x3c000000, v154
	v_rsq_f32_e32 v73, v73
	v_pk_mul_f32 v[76:77], v[142:143], v[148:149]
	v_mov_b32_e32 v80, v54
	v_mov_b32_e32 v81, v50
	v_mul_f32_e32 v78, v158, v73
	v_mov_b32_e32 v84, v58
	v_mov_b32_e32 v85, v62
	v_pk_fma_f32 v[76:77], v[144:145], v[146:147], v[76:77]
	v_pk_mul_f32 v[80:81], v[80:81], v[78:79] op_sel_hi:[1,0]
	v_pk_mul_f32 v[78:79], v[84:85], v[78:79] op_sel_hi:[1,0]
	v_pk_fma_f32 v[74:75], v[142:143], v[146:147], v[150:151] neg_lo:[0,0,1] neg_hi:[0,0,1]
	v_pk_mul_f32 v[84:85], v[76:77], v[78:79]
	v_mov_b32_e32 v62, v59
	v_pk_fma_f32 v[84:85], v[74:75], v[80:81], v[84:85]
	v_pk_mul_f32 v[80:81], v[76:77], v[80:81]
	v_cvt_pk_f16_f32 v50, v84, v85
	v_pk_fma_f32 v[78:79], v[74:75], v[78:79], v[80:81] neg_lo:[0,0,1] neg_hi:[0,0,1]
	v_pk_mul_f32 v[80:81], v[132:133], v[76:77]
	v_cvt_pk_f16_f32 v54, v78, v79
	ds_write2_b32 v118, v50, v54 offset1:32
	s_waitcnt lgkmcnt(5)
	v_add_f32_e32 v50, v83, v86
	v_fmamk_f32 v50, v50, 0x3c000000, v154
	v_rsq_f32_e32 v50, v50
	v_pk_mul_f32 v[78:79], v[134:135], v[76:77]
	v_pk_fma_f32 v[80:81], v[134:135], v[74:75], v[80:81]
	v_pk_fma_f32 v[78:79], v[132:133], v[74:75], v[78:79] neg_lo:[0,0,1] neg_hi:[0,0,1]
	v_mul_f32_e32 v54, v158, v50
	v_mov_b32_e32 v50, v55
	v_pk_mul_f32 v[50:51], v[50:51], v[54:55] op_sel_hi:[1,0]
	v_pk_mul_f32 v[54:55], v[62:63], v[54:55] op_sel_hi:[1,0]
	v_mov_b32_e32 v62, v56
	v_pk_mul_f32 v[58:59], v[80:81], v[54:55]
	v_mov_b32_e32 v63, v52
	v_pk_fma_f32 v[58:59], v[78:79], v[50:51], v[58:59]
	v_pk_mul_f32 v[50:51], v[80:81], v[50:51]
	v_cvt_pk_f16_f32 v58, v58, v59
	v_pk_fma_f32 v[50:51], v[78:79], v[54:55], v[50:51] neg_lo:[0,0,1] neg_hi:[0,0,1]
	s_waitcnt lgkmcnt(3)
	v_add_f32_e32 v54, v87, v88
	v_cvt_pk_f16_f32 v50, v50, v51
	v_fmamk_f32 v54, v54, 0x3c000000, v154
	ds_write2_b32 v114, v58, v50 offset0:68 offset1:100
	v_rsq_f32_e32 v58, v54
	v_pk_mul_f32 v[50:51], v[134:135], v[80:81]
	v_pk_mul_f32 v[54:55], v[132:133], v[80:81]
	v_pk_fma_f32 v[50:51], v[132:133], v[78:79], v[50:51] neg_lo:[0,0,1] neg_hi:[0,0,1]
	v_pk_fma_f32 v[54:55], v[134:135], v[78:79], v[54:55]
	v_mul_f32_e32 v58, v158, v58
	v_mov_b32_e32 v78, v60
	v_mov_b32_e32 v79, v64
	v_pk_mul_f32 v[62:63], v[62:63], v[58:59] op_sel_hi:[1,0]
	v_pk_mul_f32 v[58:59], v[78:79], v[58:59] op_sel_hi:[1,0]
	v_mov_b32_e32 v64, v61
	v_pk_mul_f32 v[78:79], v[54:55], v[58:59]
	s_nop 0
	v_pk_fma_f32 v[78:79], v[50:51], v[62:63], v[78:79]
	v_pk_mul_f32 v[62:63], v[54:55], v[62:63]
	v_cvt_pk_f16_f32 v52, v78, v79
	v_pk_fma_f32 v[58:59], v[50:51], v[58:59], v[62:63] neg_lo:[0,0,1] neg_hi:[0,0,1]
	s_nop 0
	v_cvt_pk_f16_f32 v56, v58, v59
	ds_write2_b32 v114, v52, v56 offset0:136 offset1:168
	s_waitcnt lgkmcnt(3)
	v_add_f32_e32 v52, v89, v90
	v_fmamk_f32 v52, v52, 0x3c000000, v154
	v_rsq_f32_e32 v52, v52
	v_pk_mul_f32 v[58:59], v[134:135], v[54:55]
	v_pk_mul_f32 v[54:55], v[132:133], v[54:55]
	v_pk_fma_f32 v[58:59], v[132:133], v[50:51], v[58:59] neg_lo:[0,0,1] neg_hi:[0,0,1]
	v_pk_fma_f32 v[50:51], v[134:135], v[50:51], v[54:55]
	v_mul_f32_e32 v54, v158, v52
	v_mov_b32_e32 v52, v57
	v_pk_mul_f32 v[52:53], v[52:53], v[54:55] op_sel_hi:[1,0]
	v_pk_mul_f32 v[54:55], v[64:65], v[54:55] op_sel_hi:[1,0]
	s_nop 0
	v_pk_mul_f32 v[56:57], v[50:51], v[54:55]
	v_pk_mul_f32 v[50:51], v[50:51], v[52:53]
	v_pk_fma_f32 v[56:57], v[58:59], v[52:53], v[56:57]
	v_pk_fma_f32 v[50:51], v[58:59], v[54:55], v[50:51] neg_lo:[0,0,1] neg_hi:[0,0,1]
	v_cvt_pk_f16_f32 v56, v56, v57
	v_cvt_pk_f16_f32 v50, v50, v51
	v_lshlrev_b32_e32 v52, 2, v166
	ds_write2_b32 v114, v56, v50 offset0:204 offset1:236
	v_or_b32_e32 v53, v52, v1
	v_bitop3_b32 v52, v52, 1, v1 bitop3:0x36
	v_lshlrev_b32_e32 v54, 2, v169
	v_lshlrev_b32_e32 v56, 2, v168
	v_lshlrev_b32_e32 v58, 2, v167
	v_lshl_add_u32 v53, v53, 2, 0
	v_lshl_add_u32 v52, v52, 2, 0
	v_or_b32_e32 v55, v54, v1
	v_bitop3_b32 v54, v54, 1, v1 bitop3:0x36
	v_or_b32_e32 v57, v56, v1
	v_bitop3_b32 v56, v56, 1, v1 bitop3:0x36
	v_or_b32_e32 v59, v58, v1
	v_bitop3_b32 v58, v58, 1, v1 bitop3:0x36
	v_lshl_add_u32 v55, v55, 2, 0
	v_lshl_add_u32 v54, v54, 2, 0
	v_lshl_add_u32 v57, v57, 2, 0
	v_lshl_add_u32 v56, v56, 2, 0
	v_lshl_add_u32 v59, v59, 2, 0
	v_lshl_add_u32 v58, v58, 2, 0
	ds_read_b32 v53, v53
	ds_read_b32 v52, v52
	ds_read_b32 v60, v55
	ds_read_b32 v61, v54
	ds_read_b32 v62, v57
	ds_read_b32 v63, v56
	ds_read_b32 v64, v59
	ds_read_b32 v65, v58
	s_waitcnt lgkmcnt(6)
	v_add_f32_e32 v52, v53, v52
	v_fmamk_f32 v52, v52, 0x3c000000, v154
	v_rsq_f32_e32 v54, v52
	v_pk_mul_f32 v[52:53], v[138:139], v[76:77]
	v_and_or_b32 v55, v166, s1, v161
	v_mov_b32_e32 v56, v38
	v_mul_f32_e32 v54, v158, v54
	v_mov_b32_e32 v57, v34
	v_mov_b32_e32 v58, v42
	v_mov_b32_e32 v59, v46
	v_pk_mul_f32 v[50:51], v[140:141], v[76:77]
	v_pk_fma_f32 v[52:53], v[140:141], v[74:75], v[52:53]
	v_mad_u32_u24 v73, v55, s0, v162
	v_pk_mul_f32 v[56:57], v[56:57], v[54:55] op_sel_hi:[1,0]
	v_pk_mul_f32 v[54:55], v[58:59], v[54:55] op_sel_hi:[1,0]
	v_pk_fma_f32 v[50:51], v[138:139], v[74:75], v[50:51] neg_lo:[0,0,1] neg_hi:[0,0,1]
	v_pk_mul_f32 v[58:59], v[52:53], v[54:55]
	v_add_u32_e32 v42, 0x1000, v73
	v_pk_fma_f32 v[58:59], v[50:51], v[56:57], v[58:59]
	v_pk_mul_f32 v[56:57], v[52:53], v[56:57]
	v_cvt_pk_f16_f32 v34, v58, v59
	v_pk_fma_f32 v[54:55], v[50:51], v[54:55], v[56:57] neg_lo:[0,0,1] neg_hi:[0,0,1]
	v_pk_mul_f32 v[56:57], v[132:133], v[52:53]
	v_cvt_pk_f16_f32 v38, v54, v55
	ds_write2_b32 v42, v34, v38 offset1:32
	s_waitcnt lgkmcnt(5)
	v_add_f32_e32 v34, v60, v61
	v_fmamk_f32 v34, v34, 0x3c000000, v154
	v_rsq_f32_e32 v34, v34
	v_mov_b32_e32 v46, v43
	v_pk_mul_f32 v[54:55], v[134:135], v[52:53]
	v_pk_fma_f32 v[56:57], v[134:135], v[50:51], v[56:57]
	v_mul_f32_e32 v38, v158, v34
	v_mov_b32_e32 v34, v39
	v_pk_mul_f32 v[34:35], v[34:35], v[38:39] op_sel_hi:[1,0]
	v_pk_mul_f32 v[38:39], v[46:47], v[38:39] op_sel_hi:[1,0]
	v_pk_fma_f32 v[54:55], v[132:133], v[50:51], v[54:55] neg_lo:[0,0,1] neg_hi:[0,0,1]
	v_pk_mul_f32 v[42:43], v[56:57], v[38:39]
	v_mov_b32_e32 v46, v40
	v_pk_fma_f32 v[42:43], v[54:55], v[34:35], v[42:43]
	v_pk_mul_f32 v[34:35], v[56:57], v[34:35]
	v_cvt_pk_f16_f32 v42, v42, v43
	v_pk_fma_f32 v[34:35], v[54:55], v[38:39], v[34:35] neg_lo:[0,0,1] neg_hi:[0,0,1]
	s_waitcnt lgkmcnt(3)
	v_add_f32_e32 v38, v62, v63
	v_cvt_pk_f16_f32 v34, v34, v35
	v_fmamk_f32 v38, v38, 0x3c000000, v154
	ds_write2_b32 v98, v42, v34 offset0:68 offset1:100
	v_rsq_f32_e32 v42, v38
	v_pk_mul_f32 v[34:35], v[134:135], v[56:57]
	v_pk_mul_f32 v[38:39], v[132:133], v[56:57]
	v_pk_fma_f32 v[34:35], v[132:133], v[54:55], v[34:35] neg_lo:[0,0,1] neg_hi:[0,0,1]
	v_pk_fma_f32 v[38:39], v[134:135], v[54:55], v[38:39]
	v_mul_f32_e32 v42, v158, v42
	v_mov_b32_e32 v47, v36
	v_mov_b32_e32 v54, v44
	v_mov_b32_e32 v55, v48
	v_pk_mul_f32 v[46:47], v[46:47], v[42:43] op_sel_hi:[1,0]
	v_pk_mul_f32 v[42:43], v[54:55], v[42:43] op_sel_hi:[1,0]
	v_mov_b32_e32 v48, v45
	v_pk_mul_f32 v[54:55], v[38:39], v[42:43]
	s_nop 0
	v_pk_fma_f32 v[54:55], v[34:35], v[46:47], v[54:55]
	v_pk_mul_f32 v[46:47], v[38:39], v[46:47]
	v_cvt_pk_f16_f32 v36, v54, v55
	v_pk_fma_f32 v[42:43], v[34:35], v[42:43], v[46:47] neg_lo:[0,0,1] neg_hi:[0,0,1]
	s_nop 0
	v_cvt_pk_f16_f32 v40, v42, v43
	ds_write2_b32 v98, v36, v40 offset0:136 offset1:168
	s_waitcnt lgkmcnt(3)
	v_add_f32_e32 v36, v64, v65
	v_fmamk_f32 v36, v36, 0x3c000000, v154
	v_rsq_f32_e32 v36, v36
	v_pk_mul_f32 v[42:43], v[134:135], v[38:39]
	v_pk_mul_f32 v[38:39], v[132:133], v[38:39]
	v_pk_fma_f32 v[42:43], v[132:133], v[34:35], v[42:43] neg_lo:[0,0,1] neg_hi:[0,0,1]
	v_pk_fma_f32 v[34:35], v[134:135], v[34:35], v[38:39]
	v_mul_f32_e32 v38, v158, v36
	v_mov_b32_e32 v36, v41
	v_pk_mul_f32 v[36:37], v[36:37], v[38:39] op_sel_hi:[1,0]
	v_pk_mul_f32 v[38:39], v[48:49], v[38:39] op_sel_hi:[1,0]
	s_nop 0
	v_pk_mul_f32 v[40:41], v[34:35], v[38:39]
	v_pk_mul_f32 v[34:35], v[34:35], v[36:37]
	v_pk_fma_f32 v[40:41], v[42:43], v[36:37], v[40:41]
	v_pk_fma_f32 v[34:35], v[42:43], v[38:39], v[34:35] neg_lo:[0,0,1] neg_hi:[0,0,1]
	v_cvt_pk_f16_f32 v40, v40, v41
	v_cvt_pk_f16_f32 v34, v34, v35
	v_lshlrev_b32_e32 v36, 2, v160
	ds_write2_b32 v98, v40, v34 offset0:204 offset1:236
	v_or_b32_e32 v37, v36, v1
	v_bitop3_b32 v36, v36, 1, v1 bitop3:0x36
	v_lshlrev_b32_e32 v38, 2, v165
	v_lshlrev_b32_e32 v40, 2, v164
	v_lshlrev_b32_e32 v42, 2, v163
	v_lshl_add_u32 v37, v37, 2, 0
	v_lshl_add_u32 v36, v36, 2, 0
	v_or_b32_e32 v39, v38, v1
	v_bitop3_b32 v38, v38, 1, v1 bitop3:0x36
	v_or_b32_e32 v41, v40, v1
	v_bitop3_b32 v40, v40, 1, v1 bitop3:0x36
	v_or_b32_e32 v43, v42, v1
	v_bitop3_b32 v42, v42, 1, v1 bitop3:0x36
	v_lshl_add_u32 v39, v39, 2, 0
	v_lshl_add_u32 v38, v38, 2, 0
	v_lshl_add_u32 v41, v41, 2, 0
	v_lshl_add_u32 v40, v40, 2, 0
	v_lshl_add_u32 v43, v43, 2, 0
	v_lshl_add_u32 v42, v42, 2, 0
	ds_read_b32 v37, v37
	ds_read_b32 v36, v36
	ds_read_b32 v44, v39
	ds_read_b32 v45, v38
	ds_read_b32 v46, v41
	ds_read_b32 v47, v40
	ds_read_b32 v48, v43
	ds_read_b32 v49, v42
	s_waitcnt lgkmcnt(6)
	v_add_f32_e32 v36, v37, v36
	v_fmamk_f32 v36, v36, 0x3c000000, v154
	v_rsq_f32_e32 v38, v36
	v_pk_mul_f32 v[34:35], v[140:141], v[52:53]
	v_pk_mul_f32 v[36:37], v[138:139], v[52:53]
	v_and_or_b32 v39, v160, s3, v161
	v_mul_f32_e32 v38, v158, v38
	v_mov_b32_e32 v40, v22
	v_mov_b32_e32 v41, v18
	v_mov_b32_e32 v42, v26
	v_mov_b32_e32 v43, v30
	v_pk_fma_f32 v[34:35], v[138:139], v[50:51], v[34:35] neg_lo:[0,0,1] neg_hi:[0,0,1]
	v_pk_fma_f32 v[36:37], v[140:141], v[50:51], v[36:37]
	v_mad_u32_u24 v50, v39, s0, v162
	v_pk_mul_f32 v[40:41], v[40:41], v[38:39] op_sel_hi:[1,0]
	v_pk_mul_f32 v[38:39], v[42:43], v[38:39] op_sel_hi:[1,0]
	v_add_u32_e32 v26, 0x1000, v50
	v_pk_mul_f32 v[42:43], v[36:37], v[38:39]
	v_mov_b32_e32 v30, v27
	v_pk_fma_f32 v[42:43], v[34:35], v[40:41], v[42:43]
	v_pk_mul_f32 v[40:41], v[36:37], v[40:41]
	v_cvt_pk_f16_f32 v18, v42, v43
	v_pk_fma_f32 v[38:39], v[34:35], v[38:39], v[40:41] neg_lo:[0,0,1] neg_hi:[0,0,1]
	v_pk_mul_f32 v[40:41], v[132:133], v[36:37]
	v_cvt_pk_f16_f32 v22, v38, v39
	ds_write2_b32 v26, v18, v22 offset1:32
	s_waitcnt lgkmcnt(5)
	v_add_f32_e32 v18, v44, v45
	v_fmamk_f32 v18, v18, 0x3c000000, v154
	v_rsq_f32_e32 v18, v18
	v_pk_mul_f32 v[38:39], v[134:135], v[36:37]
	v_pk_fma_f32 v[40:41], v[134:135], v[34:35], v[40:41]
	v_pk_fma_f32 v[38:39], v[132:133], v[34:35], v[38:39] neg_lo:[0,0,1] neg_hi:[0,0,1]
	v_mul_f32_e32 v22, v158, v18
	v_mov_b32_e32 v18, v23
	v_pk_mul_f32 v[18:19], v[18:19], v[22:23] op_sel_hi:[1,0]
	v_pk_mul_f32 v[22:23], v[30:31], v[22:23] op_sel_hi:[1,0]
	v_mov_b32_e32 v30, v24
	v_pk_mul_f32 v[26:27], v[40:41], v[22:23]
	v_mov_b32_e32 v31, v20
	v_pk_fma_f32 v[26:27], v[38:39], v[18:19], v[26:27]
	v_pk_mul_f32 v[18:19], v[40:41], v[18:19]
	v_cvt_pk_f16_f32 v26, v26, v27
	v_pk_fma_f32 v[18:19], v[38:39], v[22:23], v[18:19] neg_lo:[0,0,1] neg_hi:[0,0,1]
	s_waitcnt lgkmcnt(3)
	v_add_f32_e32 v22, v46, v47
	v_cvt_pk_f16_f32 v18, v18, v19
	v_fmamk_f32 v22, v22, 0x3c000000, v154
	ds_write2_b32 v82, v26, v18 offset0:68 offset1:100
	v_rsq_f32_e32 v26, v22
	v_pk_mul_f32 v[18:19], v[134:135], v[40:41]
	v_pk_mul_f32 v[22:23], v[132:133], v[40:41]
	v_pk_fma_f32 v[18:19], v[132:133], v[38:39], v[18:19] neg_lo:[0,0,1] neg_hi:[0,0,1]
	v_pk_fma_f32 v[22:23], v[134:135], v[38:39], v[22:23]
	v_mul_f32_e32 v26, v158, v26
	v_mov_b32_e32 v38, v28
	v_mov_b32_e32 v39, v32
	v_pk_mul_f32 v[30:31], v[30:31], v[26:27] op_sel_hi:[1,0]
	v_pk_mul_f32 v[26:27], v[38:39], v[26:27] op_sel_hi:[1,0]
	v_mov_b32_e32 v32, v29
	v_pk_mul_f32 v[38:39], v[22:23], v[26:27]
	s_nop 0
	v_pk_fma_f32 v[38:39], v[18:19], v[30:31], v[38:39]
	v_pk_mul_f32 v[30:31], v[22:23], v[30:31]
	v_cvt_pk_f16_f32 v20, v38, v39
	v_pk_fma_f32 v[26:27], v[18:19], v[26:27], v[30:31] neg_lo:[0,0,1] neg_hi:[0,0,1]
	s_nop 0
	v_cvt_pk_f16_f32 v24, v26, v27
	ds_write2_b32 v82, v20, v24 offset0:136 offset1:168
	s_waitcnt lgkmcnt(3)
	v_add_f32_e32 v20, v48, v49
	v_fmamk_f32 v20, v20, 0x3c000000, v154
	v_rsq_f32_e32 v20, v20
	v_pk_mul_f32 v[26:27], v[134:135], v[22:23]
	v_pk_mul_f32 v[22:23], v[132:133], v[22:23]
	v_pk_fma_f32 v[26:27], v[132:133], v[18:19], v[26:27] neg_lo:[0,0,1] neg_hi:[0,0,1]
	v_pk_fma_f32 v[18:19], v[134:135], v[18:19], v[22:23]
	v_mul_f32_e32 v22, v158, v20
	v_mov_b32_e32 v20, v25
	v_pk_mul_f32 v[20:21], v[20:21], v[22:23] op_sel_hi:[1,0]
	v_pk_mul_f32 v[22:23], v[32:33], v[22:23] op_sel_hi:[1,0]
	s_nop 0
	v_pk_mul_f32 v[24:25], v[18:19], v[22:23]
	v_pk_mul_f32 v[18:19], v[18:19], v[20:21]
	v_pk_fma_f32 v[24:25], v[26:27], v[20:21], v[24:25]
	v_pk_fma_f32 v[18:19], v[26:27], v[22:23], v[18:19] neg_lo:[0,0,1] neg_hi:[0,0,1]
	v_cvt_pk_f16_f32 v24, v24, v25
	v_cvt_pk_f16_f32 v18, v18, v19
	ds_write2_b32 v82, v24, v18 offset0:204 offset1:236
	v_lshlrev_b32_e32 v20, 2, v153
	v_lshlrev_b32_e32 v22, 2, v159
	v_lshlrev_b32_e32 v24, 2, v157
	v_lshlrev_b32_e32 v26, 2, v156
	v_or_b32_e32 v21, v20, v1
	v_bitop3_b32 v20, v20, 1, v1 bitop3:0x36
	v_or_b32_e32 v23, v22, v1
	v_bitop3_b32 v22, v22, 1, v1 bitop3:0x36
	v_or_b32_e32 v25, v24, v1
	v_bitop3_b32 v24, v24, 1, v1 bitop3:0x36
	v_or_b32_e32 v27, v26, v1
	v_bitop3_b32 v1, v26, 1, v1 bitop3:0x36
	v_lshl_add_u32 v21, v21, 2, 0
	v_lshl_add_u32 v20, v20, 2, 0
	v_lshl_add_u32 v1, v1, 2, 0
	v_lshl_add_u32 v23, v23, 2, 0
	v_lshl_add_u32 v22, v22, 2, 0
	v_lshl_add_u32 v25, v25, 2, 0
	v_lshl_add_u32 v24, v24, 2, 0
	v_lshl_add_u32 v27, v27, 2, 0
	ds_read_b32 v21, v21
	ds_read_b32 v20, v20
	ds_read_b32 v28, v23
	ds_read_b32 v29, v22
	ds_read_b32 v30, v25
	ds_read_b32 v31, v24
	ds_read_b32 v32, v27
	ds_read_b32 v1, v1
	s_waitcnt lgkmcnt(6)
	v_add_f32_e32 v20, v21, v20
	v_fmamk_f32 v20, v20, 0x3c000000, v154
	v_rsq_f32_e32 v22, v20
	v_pk_mul_f32 v[20:21], v[138:139], v[36:37]
	v_and_or_b32 v23, v153, s4, v161
	v_mov_b32_e32 v24, v6
	v_mul_f32_e32 v22, v158, v22
	v_mov_b32_e32 v25, v2
	v_mov_b32_e32 v26, v10
	v_mov_b32_e32 v27, v14
	v_pk_mul_f32 v[18:19], v[140:141], v[36:37]
	v_pk_fma_f32 v[20:21], v[140:141], v[34:35], v[20:21]
	v_mad_u32_u24 v33, v23, s0, v162
	v_pk_mul_f32 v[24:25], v[24:25], v[22:23] op_sel_hi:[1,0]
	v_pk_mul_f32 v[22:23], v[26:27], v[22:23] op_sel_hi:[1,0]
	v_pk_fma_f32 v[18:19], v[138:139], v[34:35], v[18:19] neg_lo:[0,0,1] neg_hi:[0,0,1]
	v_pk_mul_f32 v[26:27], v[20:21], v[22:23]
	v_add_u32_e32 v10, 0x1000, v33
	v_pk_fma_f32 v[26:27], v[18:19], v[24:25], v[26:27]
	v_pk_mul_f32 v[24:25], v[20:21], v[24:25]
	v_cvt_pk_f16_f32 v2, v26, v27
	v_pk_fma_f32 v[22:23], v[18:19], v[22:23], v[24:25] neg_lo:[0,0,1] neg_hi:[0,0,1]
	v_mov_b32_e32 v14, v11
	v_cvt_pk_f16_f32 v6, v22, v23
	ds_write2_b32 v10, v2, v6 offset1:32
	s_waitcnt lgkmcnt(5)
	v_add_f32_e32 v2, v28, v29
	v_fmamk_f32 v2, v2, 0x3c000000, v154
	v_rsq_f32_e32 v2, v2
	v_pk_mul_f32 v[22:23], v[134:135], v[20:21]
	v_pk_mul_f32 v[20:21], v[132:133], v[20:21]
	v_pk_fma_f32 v[22:23], v[132:133], v[18:19], v[22:23] neg_lo:[0,0,1] neg_hi:[0,0,1]
	v_mul_f32_e32 v6, v158, v2
	v_mov_b32_e32 v2, v7
	v_pk_fma_f32 v[18:19], v[134:135], v[18:19], v[20:21]
	v_pk_mul_f32 v[2:3], v[2:3], v[6:7] op_sel_hi:[1,0]
	v_pk_mul_f32 v[6:7], v[14:15], v[6:7] op_sel_hi:[1,0]
	v_mov_b32_e32 v14, v8
	v_pk_mul_f32 v[10:11], v[18:19], v[6:7]
	v_mov_b32_e32 v15, v4
	v_pk_fma_f32 v[10:11], v[22:23], v[2:3], v[10:11]
	v_pk_mul_f32 v[2:3], v[18:19], v[2:3]
	v_cvt_pk_f16_f32 v10, v10, v11
	v_pk_fma_f32 v[2:3], v[22:23], v[6:7], v[2:3] neg_lo:[0,0,1] neg_hi:[0,0,1]
	s_waitcnt lgkmcnt(3)
	v_add_f32_e32 v6, v30, v31
	v_cvt_pk_f16_f32 v2, v2, v3
	v_fmamk_f32 v6, v6, 0x3c000000, v154
	ds_write2_b32 v67, v10, v2 offset0:68 offset1:100
	v_rsq_f32_e32 v10, v6
	v_pk_mul_f32 v[2:3], v[134:135], v[18:19]
	v_pk_mul_f32 v[6:7], v[132:133], v[18:19]
	v_mov_b32_e32 v18, v12
	v_mul_f32_e32 v10, v158, v10
	v_mov_b32_e32 v19, v16
	s_waitcnt lgkmcnt(2)
	v_add_f32_e32 v1, v32, v1
	v_pk_fma_f32 v[6:7], v[134:135], v[22:23], v[6:7]
	v_pk_mul_f32 v[14:15], v[14:15], v[10:11] op_sel_hi:[1,0]
	v_pk_mul_f32 v[10:11], v[18:19], v[10:11] op_sel_hi:[1,0]
	v_fmac_f32_e32 v154, 0x3c000000, v1
	v_pk_fma_f32 v[2:3], v[132:133], v[22:23], v[2:3] neg_lo:[0,0,1] neg_hi:[0,0,1]
	v_pk_mul_f32 v[18:19], v[6:7], v[10:11]
	v_rsq_f32_e32 v1, v154
	v_pk_fma_f32 v[18:19], v[2:3], v[14:15], v[18:19]
	v_pk_mul_f32 v[14:15], v[6:7], v[14:15]
	v_cvt_pk_f16_f32 v4, v18, v19
	v_pk_fma_f32 v[10:11], v[2:3], v[10:11], v[14:15] neg_lo:[0,0,1] neg_hi:[0,0,1]
	v_mov_b32_e32 v16, v13
	v_cvt_pk_f16_f32 v8, v10, v11
	v_pk_mul_f32 v[10:11], v[134:135], v[6:7]
	v_pk_mul_f32 v[6:7], v[132:133], v[6:7]
	ds_write2_b32 v67, v4, v8 offset0:136 offset1:168
	v_pk_fma_f32 v[10:11], v[132:133], v[2:3], v[10:11] neg_lo:[0,0,1] neg_hi:[0,0,1]
	v_pk_fma_f32 v[2:3], v[134:135], v[2:3], v[6:7]
	v_mul_f32_e32 v6, v158, v1
	v_mov_b32_e32 v4, v9
	v_pk_mul_f32 v[4:5], v[4:5], v[6:7] op_sel_hi:[1,0]
	v_pk_mul_f32 v[6:7], v[16:17], v[6:7] op_sel_hi:[1,0]
	s_or_b32 s0, s2, 0x80
	v_pk_mul_f32 v[8:9], v[2:3], v[6:7]
	v_pk_mul_f32 v[2:3], v[2:3], v[4:5]
	v_pk_fma_f32 v[8:9], v[10:11], v[4:5], v[8:9]
	v_pk_fma_f32 v[2:3], v[10:11], v[6:7], v[2:3] neg_lo:[0,0,1] neg_hi:[0,0,1]
	v_cvt_pk_f16_f32 v1, v8, v9
	v_cvt_pk_f16_f32 v2, v2, v3
	ds_write2_b32 v67, v1, v2 offset0:204 offset1:236
	s_waitcnt lgkmcnt(0)
	s_barrier
	ds_read_b128 v[2:5], v155 offset:4096
	v_or_b32_e32 v1, s0, v152
	v_lshlrev_b32_e32 v130, 8, v1
	v_lshl_add_u64 v[10:11], v[136:137], 0, v[130:131]
	ds_read_b128 v[6:9], v68 offset:38912
	s_waitcnt lgkmcnt(1)
	global_store_dwordx4 v[10:11], v[2:5], off sc1
	ds_read_b128 v[2:5], v68 offset:4096
	ds_read_b128 v[10:13], v70 offset:4096
	v_or_b32_e32 v1, s0, v66
	v_lshlrev_b32_e32 v130, 8, v1
	v_or_b32_e32 v1, s0, v69
	v_lshl_add_u64 v[14:15], v[136:137], 0, v[130:131]
	v_lshlrev_b32_e32 v130, 8, v1
	s_waitcnt lgkmcnt(1)
	global_store_dwordx4 v[14:15], v[2:5], off sc1
	v_or_b32_e32 v1, s0, v0
	s_or_b32 s0, s2, 0x1080
	v_lshl_add_u64 v[2:3], v[136:137], 0, v[130:131]
	s_waitcnt lgkmcnt(0)
	global_store_dwordx4 v[2:3], v[10:13], off sc1
	ds_read_b128 v[2:5], v71 offset:4096
	ds_read_b128 v[10:13], v72 offset:4096
	v_lshlrev_b32_e32 v130, 8, v1
	v_lshl_add_u64 v[14:15], v[136:137], 0, v[130:131]
	v_or_b32_e32 v1, s0, v152
	s_waitcnt lgkmcnt(1)
	global_store_dwordx4 v[14:15], v[2:5], off sc1
	ds_read_b128 v[2:5], v155 offset:38912
	ds_read_b128 v[14:17], v155 offset:56320
	v_lshlrev_b32_e32 v130, 8, v1
	v_or_b32_e32 v1, s0, v66
	v_lshl_add_u64 v[18:19], v[136:137], 0, v[130:131]
	v_lshlrev_b32_e32 v130, 8, v1
	v_or_b32_e32 v1, s0, v69
	s_waitcnt lgkmcnt(1)
	global_store_dwordx4 v[18:19], v[2:5], off sc1
	v_or_b32_e32 v0, s0, v0
	s_nop 0
	v_lshl_add_u64 v[2:3], v[136:137], 0, v[130:131]
	v_lshlrev_b32_e32 v130, 8, v1
	global_store_dwordx4 v[2:3], v[6:9], off sc1
	v_lshl_add_u64 v[2:3], v[136:137], 0, v[130:131]
	v_lshlrev_b32_e32 v130, 8, v0
	v_lshl_add_u64 v[0:1], v[136:137], 0, v[130:131]
	s_waitcnt lgkmcnt(0)
	global_store_dwordx4 v[2:3], v[14:17], off sc1
	global_store_dwordx4 v[0:1], v[10:13], off sc1
	s_barrier
	s_endpgm

.LBB3_32:
	s_lshl_b32 s95, s33, 7
	s_or_b32 s4, s79, s95
	v_or_b32_e32 v17, s4, v17
	v_lshlrev_b32_e32 v20, 8, v17
	v_mov_b32_e32 v21, 0
	v_lshlrev_b32_e32 v18, 3, v18
	v_lshl_add_u64 v[22:23], s[64:65], 0, v[20:21]
	v_ashrrev_i32_e32 v19, 31, v18
	v_lshl_add_u64 v[18:19], v[18:19], 1, v[22:23]
	global_load_dwordx4 v[156:159], v[18:19], off
	global_load_dwordx4 v[152:155], v[18:19], off offset:32
	global_load_dwordx4 v[148:151], v[18:19], off offset:64
	global_load_dwordx4 v[144:147], v[18:19], off offset:96
	global_load_dwordx4 v[140:143], v[18:19], off offset:128
	global_load_dwordx4 v[136:139], v[18:19], off offset:160
	global_load_dwordx4 v[132:135], v[18:19], off offset:192
	global_load_dwordx4 v[128:131], v[18:19], off offset:224
	s_lshl_b32 s4, s78, 7
	s_ashr_i32 s5, s4, 31
	s_lshl_b64 s[4:5], s[4:5], 1
	s_waitcnt lgkmcnt(0)
	s_barrier
	s_add_u32 s66, s66, s4
	s_addc_u32 s67, s67, s5
	s_lshl_b32 s4, s99, 19
	s_add_u32 s4, s66, s4
	v_add_u32_e32 v30, s96, v16
	v_lshlrev_b32_e32 v16, 4, v16
	s_addc_u32 s5, s67, 0
	v_and_b32_e32 v20, 0xf0, v16
	s_add_i32 s78, 0, 0x18000
	v_add_u32_e32 v31, s78, v20
	v_lshl_add_u64 v[24:25], s[4:5], 0, v[20:21]
	v_ashrrev_i32_e32 v20, 4, v30
	v_ashrrev_i32_e32 v21, 31, v20
	v_lshl_add_u32 v16, v20, 8, v31
	v_lshlrev_b64 v[20:21], 12, v[20:21]
	v_lshl_add_u64 v[26:27], v[24:25], 0, v[20:21]
	v_add_u32_e32 v20, 0x200, v30
	ds_read_b128 v[16:19], v16
	v_ashrrev_i32_e32 v28, 4, v20
	v_lshl_add_u32 v20, v28, 8, v31
	ds_read_b128 v[20:23], v20
	v_ashrrev_i32_e32 v29, 31, v28
	s_waitcnt lgkmcnt(1)
	global_store_dwordx4 v[26:27], v[16:19], off sc1
	s_nop 1
	v_lshlrev_b64 v[16:17], 12, v[28:29]
	v_lshl_add_u64 v[16:17], v[24:25], 0, v[16:17]
	s_waitcnt lgkmcnt(0)
	global_store_dwordx4 v[16:17], v[20:23], off sc1
	v_add_u32_e32 v16, 0x400, v30
	s_nop 0
	v_ashrrev_i32_e32 v20, 4, v16
	v_ashrrev_i32_e32 v21, 31, v20
	v_lshl_add_u32 v16, v20, 8, v31
	v_lshlrev_b64 v[20:21], 12, v[20:21]
	v_lshl_add_u64 v[26:27], v[24:25], 0, v[20:21]
	v_add_u32_e32 v20, 0x600, v30
	ds_read_b128 v[16:19], v16
	v_ashrrev_i32_e32 v28, 4, v20
	v_lshl_add_u32 v20, v28, 8, v31
	ds_read_b128 v[20:23], v20
	v_ashrrev_i32_e32 v29, 31, v28
	s_waitcnt lgkmcnt(1)
	global_store_dwordx4 v[26:27], v[16:19], off sc1
	s_nop 1
	v_lshlrev_b64 v[16:17], 12, v[28:29]
	v_lshl_add_u64 v[16:17], v[24:25], 0, v[16:17]
	s_waitcnt lgkmcnt(0)
	global_store_dwordx4 v[16:17], v[20:23], off sc1
	s_waitcnt vmcnt(0) lgkmcnt(0)
	s_barrier
	s_cmp_eq_u32 s33, 0
	s_cselect_b64 s[6:7], -1, 0
	s_cmp_lg_u32 s33, 0
	s_cselect_b64 s[8:9], -1, 0
	ds_read_b128 v[32:35], v190
	ds_read_b128 v[36:39], v190 offset:8192
	s_and_b64 vcc, exec, s[6:7]
	s_waitcnt vmcnt(11) lgkmcnt(1)
	v_mfma_f32_32x32x16_f16 v[16:31], v[32:35], v[156:159], -0.5
	s_waitcnt lgkmcnt(0)
	v_mfma_f32_32x32x16_f16 v[96:111], v[36:39], v[156:159], -0.5
	s_cbranch_vccnz .LBB3_34
	s_mov_b32 s4, 0x8000
	s_mov_b32 m0, s91
	s_nop 0
	buffer_load_dwordx4 v191, s[68:71], s4 offen lds

.LBB3_74:
	s_waitcnt lgkmcnt(0)
	s_barrier
	s_lshl_b32 s0, s33, 19
	v_add_u32_e32 v14, s96, v16
	v_lshlrev_b32_e32 v0, 4, v16
	s_add_u32 s0, s66, s0
	v_and_b32_e32 v0, 0xf0, v0
	v_ashrrev_i32_e32 v4, 4, v14
	s_addc_u32 s1, s67, 0
	v_add_u32_e32 v15, s78, v0
	v_mov_b32_e32 v1, 0
	v_ashrrev_i32_e32 v5, 31, v4
	v_lshl_add_u64 v[8:9], s[0:1], 0, v[0:1]
	v_lshl_add_u32 v0, v4, 8, v15
	v_lshlrev_b64 v[4:5], 12, v[4:5]
	v_lshl_add_u64 v[10:11], v[8:9], 0, v[4:5]
	v_add_u32_e32 v4, 0x200, v14
	ds_read_b128 v[0:3], v0
	v_ashrrev_i32_e32 v12, 4, v4
	v_lshl_add_u32 v4, v12, 8, v15
	ds_read_b128 v[4:7], v4
	v_ashrrev_i32_e32 v13, 31, v12
	s_waitcnt lgkmcnt(1)
	global_store_dwordx4 v[10:11], v[0:3], off sc1
	s_nop 1
	v_lshlrev_b64 v[0:1], 12, v[12:13]
	v_lshl_add_u64 v[0:1], v[8:9], 0, v[0:1]
	s_waitcnt lgkmcnt(0)
	global_store_dwordx4 v[0:1], v[4:7], off sc1
	v_add_u32_e32 v0, 0x400, v14
	s_nop 0
	v_ashrrev_i32_e32 v4, 4, v0
	v_ashrrev_i32_e32 v5, 31, v4
	v_lshl_add_u32 v0, v4, 8, v15
	v_lshlrev_b64 v[4:5], 12, v[4:5]
	v_lshl_add_u64 v[10:11], v[8:9], 0, v[4:5]
	v_add_u32_e32 v4, 0x600, v14
	ds_read_b128 v[0:3], v0
	v_ashrrev_i32_e32 v12, 4, v4
	v_lshl_add_u32 v4, v12, 8, v15
	ds_read_b128 v[4:7], v4
	v_ashrrev_i32_e32 v13, 31, v12
	s_waitcnt lgkmcnt(1)
	global_store_dwordx4 v[10:11], v[0:3], off sc1
	s_nop 1
	v_lshlrev_b64 v[0:1], 12, v[12:13]
	v_lshl_add_u64 v[0:1], v[8:9], 0, v[0:1]
	s_waitcnt lgkmcnt(0)
	global_store_dwordx4 v[0:1], v[4:7], off sc1
	s_endpgm
